# v22 plus back-edge rotation: the K-loop counter/pointer SALU block moved in front of the loop-back barrier in the 8 GEMM K-loops
# baseline (speedup 1.0000x reference)
; #define PG8_STAGE(bufoff, gbase, voff) do { _Pragma("unroll") for (int _i = 0; _i < 2; ++_i) \
;         __builtin_amdgcn_global_load_lds((const unsigned*)((const char*)(gbase) + (voff)[_i]), (PG8_LAS unsigned*)(lds + (bufoff) + ldsw + _i * 8192), 16, 0, 0); } while (0)
; #define PG8_LDA(dst, b, h) do { _Pragma("unroll") for (int m = 0; m < 4; ++m) _Pragma("unroll") for (int k = 0; k < 2; ++k) dst[m][k] = *(const PG8_LAS bf16x8*)(lds + PG8_SA(b, h) + aoff + m * 2048 + k * 1024); } while (0)
; #define PG8_LDB(dst, b, h) do { _Pragma("unroll") for (int n = 0; n < 2; ++n) _Pragma("unroll") for (int k = 0; k < 2; ++k) dst[n][k] = *(const PG8_LAS bf16x8*)(lds + PG8_SB(b, h) + boff + n * 2048 + k * 1024); } while (0)
; #define PG8_WAIT_V(n) asm volatile("s_waitcnt vmcnt(" #n ")" ::: "memory")
; #define PG8_WAIT_L(n) asm volatile("s_waitcnt lgkmcnt(" #n ")" ::: "memory")
; #define PG8_BAR __builtin_amdgcn_s_barrier()
; #define PG8_SCHED __builtin_amdgcn_sched_barrier(0)
; template <class Epi, class Sched, bool ALIGN_EPI = false, bool SP2 = false, bool FP8 = false>
; __device__ __forceinline__ void gemm_phase(PG8_LAS unsigned char* lds, const Gemm g, const Sched& S, const Epi& E) {
;     ...
;             PG8_LDB(B0, 0, 0); PG8_LDB(B1, 0, 1); PG8_SCHED; PG8_LDA(At, 0, 0); PG8_STAGE(PG8_SA(1, 1), a1 + hstep, voffA);
;             PG8_WAIT_V(8); PG8_WAIT_L(0); PG8_BAR; PG8_MMA(0, 0, At, B0); PG8_MMA(0, 1, At, B1); PG8_BAR; PG8_SCHED;
;             PG8_LDA(At, 0, 1); PG8_STAGE(PG8_SB(0, 0), b2, voffB); PG8_STAGE(PG8_SB(0, 1), b2 + hstep, voffB); PG8_STAGE(PG8_SA(0, 0), a2, voffA);
;             PG8_WAIT_V(8); PG8_WAIT_L(0); PG8_BAR; PG8_MMA(1, 0, At, B0); PG8_MMA(1, 1, At, B1); PG8_BAR; PG8_SCHED;
.LBB0_412:
	ds_read_b128 v[146:149], v152
	ds_read_b128 v[156:159], v152 offset:1024
	ds_read_b128 v[160:163], v152 offset:2048
	ds_read_b128 v[164:167], v152 offset:3072
	ds_read_b128 v[168:171], v153
	ds_read_b128 v[172:175], v153 offset:1024
	ds_read_b128 v[176:179], v153 offset:2048
	ds_read_b128 v[180:183], v153 offset:3072
	s_add_u32 s24, s22, 0xfff80080
	s_addc_u32 s25, s23, -1
	s_cmp_eq_u32 s60, 28
	s_cselect_b32 s27, s15, s25
	s_cselect_b32 s26, s48, s24
	s_cselect_b32 s25, s13, s57
	s_cselect_b32 s24, s49, s56
	v_lshl_add_u64 v[216:217], s[22:23], 0, v[138:139]
	s_add_i32 m0, s21, 0xc000
	ds_read_b128 v[184:187], v154
	ds_read_b128 v[188:191], v154 offset:1024
	ds_read_b128 v[192:195], v154 offset:2048
	ds_read_b128 v[196:199], v154 offset:3072
	ds_read_b128 v[200:203], v154 offset:4096
	ds_read_b128 v[204:207], v154 offset:5120
	ds_read_b128 v[208:211], v154 offset:6144
	ds_read_b128 v[212:215], v154 offset:7168
	global_load_lds_dwordx4 v[216:217], off
	v_lshl_add_u64 v[216:217], s[22:23], 0, v[140:141]
	s_add_i32 m0, s21, 0xe000
	s_nop 0
	global_load_lds_dwordx4 v[216:217], off
	s_waitcnt vmcnt(8)
	s_waitcnt lgkmcnt(0)
	s_barrier
	s_setprio 1
	s_waitcnt lgkmcnt(0)
	v_mfma_f32_16x16x32_bf16 v[126:129], v[146:149], v[184:187], v[126:129]
	v_mfma_f32_16x16x32_bf16 v[122:125], v[160:163], v[184:187], v[122:125]
	v_mfma_f32_16x16x32_bf16 v[118:121], v[146:149], v[192:195], v[118:121]
	v_mfma_f32_16x16x32_bf16 v[110:113], v[160:163], v[192:195], v[110:113]
	v_mfma_f32_16x16x32_bf16 v[102:105], v[146:149], v[200:203], v[102:105]
	v_mfma_f32_16x16x32_bf16 v[94:97], v[160:163], v[200:203], v[94:97]
	v_mfma_f32_16x16x32_bf16 v[86:89], v[146:149], v[208:211], v[86:89]
	v_mfma_f32_16x16x32_bf16 v[78:81], v[160:163], v[208:211], v[78:81]
	v_mfma_f32_16x16x32_bf16 v[126:129], v[156:159], v[188:191], v[126:129]
	v_mfma_f32_16x16x32_bf16 v[122:125], v[164:167], v[188:191], v[122:125]
	v_mfma_f32_16x16x32_bf16 v[118:121], v[156:159], v[196:199], v[118:121]
	v_mfma_f32_16x16x32_bf16 v[110:113], v[164:167], v[196:199], v[110:113]
	v_mfma_f32_16x16x32_bf16 v[102:105], v[156:159], v[204:207], v[102:105]
	v_mfma_f32_16x16x32_bf16 v[94:97], v[164:167], v[204:207], v[94:97]
	v_mfma_f32_16x16x32_bf16 v[86:89], v[156:159], v[212:215], v[86:89]
	v_mfma_f32_16x16x32_bf16 v[78:81], v[164:167], v[212:215], v[78:81]
	s_setprio 0
	s_setprio 1
	v_mfma_f32_16x16x32_bf16 v[114:117], v[168:171], v[184:187], v[114:117]
	v_mfma_f32_16x16x32_bf16 v[106:109], v[176:179], v[184:187], v[106:109]
	v_mfma_f32_16x16x32_bf16 v[98:101], v[168:171], v[192:195], v[98:101]
	v_mfma_f32_16x16x32_bf16 v[90:93], v[176:179], v[192:195], v[90:93]
	v_mfma_f32_16x16x32_bf16 v[82:85], v[168:171], v[200:203], v[82:85]
	v_mfma_f32_16x16x32_bf16 v[74:77], v[176:179], v[200:203], v[74:77]
	v_mfma_f32_16x16x32_bf16 v[70:73], v[168:171], v[208:211], v[70:73]
	v_mfma_f32_16x16x32_bf16 v[66:69], v[176:179], v[208:211], v[66:69]
	v_mfma_f32_16x16x32_bf16 v[114:117], v[172:175], v[188:191], v[114:117]
	v_mfma_f32_16x16x32_bf16 v[106:109], v[180:183], v[188:191], v[106:109]
	v_mfma_f32_16x16x32_bf16 v[98:101], v[172:175], v[196:199], v[98:101]
	v_mfma_f32_16x16x32_bf16 v[90:93], v[180:183], v[196:199], v[90:93]
	v_mfma_f32_16x16x32_bf16 v[82:85], v[172:175], v[204:207], v[82:85]
	v_mfma_f32_16x16x32_bf16 v[74:77], v[180:183], v[204:207], v[74:77]
	v_mfma_f32_16x16x32_bf16 v[70:73], v[172:175], v[212:215], v[70:73]
	v_mfma_f32_16x16x32_bf16 v[66:69], v[180:183], v[212:215], v[66:69]
	s_setprio 0
	s_barrier
	s_add_i32 s61, s44, s33
	v_lshl_add_u64 v[216:217], s[24:25], 0, v[134:135]
	s_mov_b32 m0, s61
	ds_read_b128 v[184:187], v154 offset:16384
	ds_read_b128 v[188:191], v154 offset:17408
	ds_read_b128 v[192:195], v154 offset:18432
	ds_read_b128 v[196:199], v154 offset:19456
	ds_read_b128 v[200:203], v154 offset:20480
	ds_read_b128 v[204:207], v154 offset:21504
	ds_read_b128 v[208:211], v154 offset:22528
	ds_read_b128 v[212:215], v154 offset:23552
	global_load_lds_dwordx4 v[216:217], off
	s_add_i32 m0, s61, 0x2000
	s_add_u32 s62, s24, 0x80000
	v_lshl_add_u64 v[218:219], s[24:25], 0, v[130:131]
	s_addc_u32 s63, s25, 0
	s_add_i32 s61, s45, s33
	global_load_lds_dwordx4 v[218:219], off
	v_lshl_add_u64 v[220:221], s[62:63], 0, v[134:135]
	s_mov_b32 m0, s61
	v_lshl_add_u64 v[222:223], s[26:27], 0, v[132:133]
	global_load_lds_dwordx4 v[220:221], off
	v_lshl_add_u64 v[220:221], s[62:63], 0, v[130:131]
	s_add_i32 m0, s61, 0x2000
	s_nop 0
	global_load_lds_dwordx4 v[220:221], off
	v_lshl_add_u64 v[220:221], s[26:27], 0, v[136:137]
	s_mov_b32 m0, s21
	s_nop 0
	global_load_lds_dwordx4 v[220:221], off
	s_mov_b32 m0, s36
	s_nop 0
	global_load_lds_dwordx4 v[222:223], off
	s_waitcnt vmcnt(8)
	s_waitcnt lgkmcnt(0)
	s_barrier
; #define PG8_STAGE(bufoff, gbase, voff) do { _Pragma("unroll") for (int _i = 0; _i < 2; ++_i) \
;         __builtin_amdgcn_global_load_lds((const unsigned*)((const char*)(gbase) + (voff)[_i]), (PG8_LAS unsigned*)(lds + (bufoff) + ldsw + _i * 8192), 16, 0, 0); } while (0)
; #define PG8_LDA(dst, b, h) do { _Pragma("unroll") for (int m = 0; m < 4; ++m) _Pragma("unroll") for (int k = 0; k < 2; ++k) dst[m][k] = *(const PG8_LAS bf16x8*)(lds + PG8_SA(b, h) + aoff + m * 2048 + k * 1024); } while (0)
; #define PG8_LDB(dst, b, h) do { _Pragma("unroll") for (int n = 0; n < 2; ++n) _Pragma("unroll") for (int k = 0; k < 2; ++k) dst[n][k] = *(const PG8_LAS bf16x8*)(lds + PG8_SB(b, h) + boff + n * 2048 + k * 1024); } while (0)
; #define PG8_WAIT_V(n) asm volatile("s_waitcnt vmcnt(" #n ")" ::: "memory")
; #define PG8_WAIT_L(n) asm volatile("s_waitcnt lgkmcnt(" #n ")" ::: "memory")
; #define PG8_BAR __builtin_amdgcn_s_barrier()
; #define PG8_SCHED __builtin_amdgcn_sched_barrier(0)
; template <class Epi, class Sched, bool ALIGN_EPI = false, bool SP2 = false, bool FP8 = false>
; __device__ __forceinline__ void gemm_phase(PG8_LAS unsigned char* lds, const Gemm g, const Sched& S, const Epi& E) {
;     ...
;             PG8_WAIT_V(8); PG8_WAIT_L(0); PG8_BAR; PG8_MMA(1, 0, At, B0); PG8_MMA(1, 1, At, B1); PG8_BAR; PG8_SCHED;
;             PG8_LDB(B0, 1, 0); PG8_LDB(B1, 1, 1); PG8_SCHED; PG8_LDA(At, 1, 0); PG8_STAGE(PG8_SA(0, 1), a2 + hstep, voffA);
;             PG8_WAIT_V(8); PG8_WAIT_L(0); PG8_BAR; PG8_MMA(0, 0, At, B0); PG8_MMA(0, 1, At, B1); PG8_BAR; PG8_SCHED;
	s_setprio 1
	s_waitcnt lgkmcnt(0)
	v_mfma_f32_16x16x32_bf16 v[62:65], v[146:149], v[184:187], v[62:65]
	v_mfma_f32_16x16x32_bf16 v[58:61], v[160:163], v[184:187], v[58:61]
	v_mfma_f32_16x16x32_bf16 v[54:57], v[146:149], v[192:195], v[54:57]
	v_mfma_f32_16x16x32_bf16 v[46:49], v[160:163], v[192:195], v[46:49]
	v_mfma_f32_16x16x32_bf16 v[38:41], v[146:149], v[200:203], v[38:41]
	v_mfma_f32_16x16x32_bf16 v[30:33], v[160:163], v[200:203], v[30:33]
	v_mfma_f32_16x16x32_bf16 v[22:25], v[146:149], v[208:211], v[22:25]
	v_mfma_f32_16x16x32_bf16 v[14:17], v[160:163], v[208:211], v[14:17]
	v_mfma_f32_16x16x32_bf16 v[62:65], v[156:159], v[188:191], v[62:65]
	v_mfma_f32_16x16x32_bf16 v[58:61], v[164:167], v[188:191], v[58:61]
	v_mfma_f32_16x16x32_bf16 v[54:57], v[156:159], v[196:199], v[54:57]
	v_mfma_f32_16x16x32_bf16 v[46:49], v[164:167], v[196:199], v[46:49]
	v_mfma_f32_16x16x32_bf16 v[38:41], v[156:159], v[204:207], v[38:41]
	v_mfma_f32_16x16x32_bf16 v[30:33], v[164:167], v[204:207], v[30:33]
	v_mfma_f32_16x16x32_bf16 v[22:25], v[156:159], v[212:215], v[22:25]
	v_mfma_f32_16x16x32_bf16 v[14:17], v[164:167], v[212:215], v[14:17]
	s_setprio 0
	s_setprio 1
	v_mfma_f32_16x16x32_bf16 v[50:53], v[168:171], v[184:187], v[50:53]
	v_mfma_f32_16x16x32_bf16 v[42:45], v[176:179], v[184:187], v[42:45]
	v_mfma_f32_16x16x32_bf16 v[34:37], v[168:171], v[192:195], v[34:37]
	v_mfma_f32_16x16x32_bf16 v[26:29], v[176:179], v[192:195], v[26:29]
	v_mfma_f32_16x16x32_bf16 v[18:21], v[168:171], v[200:203], v[18:21]
	v_mfma_f32_16x16x32_bf16 v[10:13], v[176:179], v[200:203], v[10:13]
	v_mfma_f32_16x16x32_bf16 v[6:9], v[168:171], v[208:211], v[6:9]
	v_mfma_f32_16x16x32_bf16 v[2:5], v[176:179], v[208:211], v[2:5]
	v_mfma_f32_16x16x32_bf16 v[50:53], v[172:175], v[188:191], v[50:53]
	v_mfma_f32_16x16x32_bf16 v[42:45], v[180:183], v[188:191], v[42:45]
	v_mfma_f32_16x16x32_bf16 v[34:37], v[172:175], v[196:199], v[34:37]
	v_mfma_f32_16x16x32_bf16 v[26:29], v[180:183], v[196:199], v[26:29]
	v_mfma_f32_16x16x32_bf16 v[18:21], v[172:175], v[204:207], v[18:21]
	v_mfma_f32_16x16x32_bf16 v[10:13], v[180:183], v[204:207], v[10:13]
	v_mfma_f32_16x16x32_bf16 v[6:9], v[172:175], v[212:215], v[6:9]
	v_mfma_f32_16x16x32_bf16 v[2:5], v[180:183], v[212:215], v[2:5]
	s_setprio 0
	s_barrier
	s_add_i32 s61, 0, 0x18000
	v_add_u32_e32 v155, s61, v150
	s_add_i32 s62, 0, 0x1c000
	ds_read_b128 v[146:149], v155
	ds_read_b128 v[156:159], v155 offset:1024
	ds_read_b128 v[160:163], v155 offset:2048
	ds_read_b128 v[164:167], v155 offset:3072
	v_add_u32_e32 v155, s62, v150
	ds_read_b128 v[168:171], v155
	ds_read_b128 v[172:175], v155 offset:1024
	ds_read_b128 v[176:179], v155 offset:2048
	ds_read_b128 v[180:183], v155 offset:3072
	s_add_u32 s26, s26, 0x80000
	s_addc_u32 s27, s27, 0
	s_mov_b32 m0, s37
	v_lshl_add_u64 v[224:225], s[26:27], 0, v[136:137]
	ds_read_b128 v[184:187], v154 offset:32768
	ds_read_b128 v[188:191], v154 offset:33792
	ds_read_b128 v[192:195], v154 offset:34816
	ds_read_b128 v[196:199], v154 offset:35840
	ds_read_b128 v[200:203], v154 offset:36864
	ds_read_b128 v[204:207], v154 offset:37888
	ds_read_b128 v[208:211], v154 offset:38912
	ds_read_b128 v[212:215], v154 offset:39936
	global_load_lds_dwordx4 v[224:225], off
	v_lshl_add_u64 v[224:225], s[26:27], 0, v[132:133]
	s_mov_b32 m0, s38
	s_nop 0
	global_load_lds_dwordx4 v[224:225], off
	s_waitcnt vmcnt(8)
	s_waitcnt lgkmcnt(0)
	s_barrier
	s_setprio 1
	s_waitcnt lgkmcnt(0)
	v_mfma_f32_16x16x32_bf16 v[126:129], v[146:149], v[184:187], v[126:129]
	v_mfma_f32_16x16x32_bf16 v[122:125], v[160:163], v[184:187], v[122:125]
	v_mfma_f32_16x16x32_bf16 v[118:121], v[146:149], v[192:195], v[118:121]
	v_mfma_f32_16x16x32_bf16 v[110:113], v[160:163], v[192:195], v[110:113]
	v_mfma_f32_16x16x32_bf16 v[102:105], v[146:149], v[200:203], v[102:105]
	v_mfma_f32_16x16x32_bf16 v[94:97], v[160:163], v[200:203], v[94:97]
	v_mfma_f32_16x16x32_bf16 v[86:89], v[146:149], v[208:211], v[86:89]
	v_mfma_f32_16x16x32_bf16 v[78:81], v[160:163], v[208:211], v[78:81]
	v_mfma_f32_16x16x32_bf16 v[126:129], v[156:159], v[188:191], v[126:129]
	v_mfma_f32_16x16x32_bf16 v[122:125], v[164:167], v[188:191], v[122:125]
	v_mfma_f32_16x16x32_bf16 v[118:121], v[156:159], v[196:199], v[118:121]
	v_mfma_f32_16x16x32_bf16 v[110:113], v[164:167], v[196:199], v[110:113]
	v_mfma_f32_16x16x32_bf16 v[102:105], v[156:159], v[204:207], v[102:105]
	v_mfma_f32_16x16x32_bf16 v[94:97], v[164:167], v[204:207], v[94:97]
	v_mfma_f32_16x16x32_bf16 v[86:89], v[156:159], v[212:215], v[86:89]
	v_mfma_f32_16x16x32_bf16 v[78:81], v[164:167], v[212:215], v[78:81]
	s_setprio 0
	s_setprio 1
	v_mfma_f32_16x16x32_bf16 v[114:117], v[168:171], v[184:187], v[114:117]
	v_mfma_f32_16x16x32_bf16 v[106:109], v[176:179], v[184:187], v[106:109]
	v_mfma_f32_16x16x32_bf16 v[98:101], v[168:171], v[192:195], v[98:101]
	v_mfma_f32_16x16x32_bf16 v[90:93], v[176:179], v[192:195], v[90:93]
	v_mfma_f32_16x16x32_bf16 v[82:85], v[168:171], v[200:203], v[82:85]
	v_mfma_f32_16x16x32_bf16 v[74:77], v[176:179], v[200:203], v[74:77]
	v_mfma_f32_16x16x32_bf16 v[70:73], v[168:171], v[208:211], v[70:73]
	v_mfma_f32_16x16x32_bf16 v[66:69], v[176:179], v[208:211], v[66:69]
	v_mfma_f32_16x16x32_bf16 v[114:117], v[172:175], v[188:191], v[114:117]
	v_mfma_f32_16x16x32_bf16 v[106:109], v[180:183], v[188:191], v[106:109]
	v_mfma_f32_16x16x32_bf16 v[98:101], v[172:175], v[196:199], v[98:101]
	v_mfma_f32_16x16x32_bf16 v[90:93], v[180:183], v[196:199], v[90:93]
	v_mfma_f32_16x16x32_bf16 v[82:85], v[172:175], v[204:207], v[82:85]
	v_mfma_f32_16x16x32_bf16 v[74:77], v[180:183], v[204:207], v[74:77]
	v_mfma_f32_16x16x32_bf16 v[70:73], v[172:175], v[212:215], v[70:73]
	v_mfma_f32_16x16x32_bf16 v[66:69], v[180:183], v[212:215], v[66:69]
	s_setprio 0
	s_barrier
; #define PG8_STAGE(bufoff, gbase, voff) do { _Pragma("unroll") for (int _i = 0; _i < 2; ++_i) \
;         __builtin_amdgcn_global_load_lds((const unsigned*)((const char*)(gbase) + (voff)[_i]), (PG8_LAS unsigned*)(lds + (bufoff) + ldsw + _i * 8192), 16, 0, 0); } while (0)
; #define PG8_LDA(dst, b, h) do { _Pragma("unroll") for (int m = 0; m < 4; ++m) _Pragma("unroll") for (int k = 0; k < 2; ++k) dst[m][k] = *(const PG8_LAS bf16x8*)(lds + PG8_SA(b, h) + aoff + m * 2048 + k * 1024); } while (0)
; #define PG8_WAIT_V(n) asm volatile("s_waitcnt vmcnt(" #n ")" ::: "memory")
; #define PG8_WAIT_L(n) asm volatile("s_waitcnt lgkmcnt(" #n ")" ::: "memory")
; #define PG8_BAR __builtin_amdgcn_s_barrier()
; #define PG8_SCHED __builtin_amdgcn_sched_barrier(0)
; template <class Epi, class Sched, bool ALIGN_EPI = false, bool SP2 = false, bool FP8 = false>
; __device__ __forceinline__ void gemm_phase(PG8_LAS unsigned char* lds, const Gemm g, const Sched& S, const Epi& E) {
;     ...
;         for (int t = 0; t < nt; t += 2) {
;             const bool last = (t == nt - 2);
;             const char* a1 = cA + (size_t)(t + 1) * kstep;
;             const char* a2 = last ? nA : cA + (size_t)(t + 2) * kstep; const char* b2 = last ? nB : cB + (size_t)(t + 2) * kstep;
;     ...
;             PG8_LDA(At, 1, 1); PG8_STAGE(PG8_SB(1, 0), b3, voffB); PG8_STAGE(PG8_SB(1, 1), b3 + hstep, voffB); PG8_STAGE(PG8_SA(1, 0), a3, voffA);
;             PG8_WAIT_V(8); PG8_WAIT_L(0); PG8_BAR; PG8_MMA(1, 0, At, B0); PG8_MMA(1, 1, At, B1); PG8_BAR; PG8_SCHED;
	s_add_i32 s26, s61, s33
	v_lshl_add_u64 v[216:217], v[216:217], 0, s[8:9]
	s_mov_b32 m0, s26
	ds_read_b128 v[184:187], v154 offset:49152
	ds_read_b128 v[188:191], v154 offset:50176
	ds_read_b128 v[192:195], v154 offset:51200
	ds_read_b128 v[196:199], v154 offset:52224
	ds_read_b128 v[200:203], v154 offset:53248
	ds_read_b128 v[204:207], v154 offset:54272
	ds_read_b128 v[208:211], v154 offset:55296
	ds_read_b128 v[212:215], v154 offset:56320
	global_load_lds_dwordx4 v[216:217], off
	s_add_i32 m0, s26, 0x2000
	s_add_u32 s24, s24, 0x80080
	v_lshl_add_u64 v[216:217], v[218:219], 0, s[8:9]
	s_addc_u32 s25, s25, 0
	s_add_i32 s26, s62, s33
	global_load_lds_dwordx4 v[216:217], off
	v_lshl_add_u64 v[216:217], s[24:25], 0, v[134:135]
	s_mov_b32 m0, s26
	s_nop 0
	global_load_lds_dwordx4 v[216:217], off
	v_lshl_add_u64 v[216:217], s[24:25], 0, v[130:131]
	s_add_i32 m0, s26, 0x2000
	s_nop 0
	global_load_lds_dwordx4 v[216:217], off
	v_lshl_add_u64 v[216:217], v[220:221], 0, s[8:9]
	s_mov_b32 m0, s41
	s_nop 0
	global_load_lds_dwordx4 v[216:217], off
	v_lshl_add_u64 v[216:217], v[222:223], 0, s[8:9]
	s_mov_b32 m0, s42
	s_nop 0
	global_load_lds_dwordx4 v[216:217], off
	s_waitcnt vmcnt(8)
	s_waitcnt lgkmcnt(0)
	s_barrier
	s_setprio 1
	s_waitcnt lgkmcnt(0)
	v_mfma_f32_16x16x32_bf16 v[62:65], v[146:149], v[184:187], v[62:65]
	v_mfma_f32_16x16x32_bf16 v[58:61], v[160:163], v[184:187], v[58:61]
	v_mfma_f32_16x16x32_bf16 v[54:57], v[146:149], v[192:195], v[54:57]
	v_mfma_f32_16x16x32_bf16 v[46:49], v[160:163], v[192:195], v[46:49]
	v_mfma_f32_16x16x32_bf16 v[38:41], v[146:149], v[200:203], v[38:41]
	v_mfma_f32_16x16x32_bf16 v[30:33], v[160:163], v[200:203], v[30:33]
	v_mfma_f32_16x16x32_bf16 v[22:25], v[146:149], v[208:211], v[22:25]
	v_mfma_f32_16x16x32_bf16 v[14:17], v[160:163], v[208:211], v[14:17]
	v_mfma_f32_16x16x32_bf16 v[62:65], v[156:159], v[188:191], v[62:65]
	v_mfma_f32_16x16x32_bf16 v[58:61], v[164:167], v[188:191], v[58:61]
	v_mfma_f32_16x16x32_bf16 v[54:57], v[156:159], v[196:199], v[54:57]
	v_mfma_f32_16x16x32_bf16 v[46:49], v[164:167], v[196:199], v[46:49]
	v_mfma_f32_16x16x32_bf16 v[38:41], v[156:159], v[204:207], v[38:41]
	v_mfma_f32_16x16x32_bf16 v[30:33], v[164:167], v[204:207], v[30:33]
	v_mfma_f32_16x16x32_bf16 v[22:25], v[156:159], v[212:215], v[22:25]
	v_mfma_f32_16x16x32_bf16 v[14:17], v[164:167], v[212:215], v[14:17]
	s_setprio 0
	s_setprio 1
	v_mfma_f32_16x16x32_bf16 v[50:53], v[168:171], v[184:187], v[50:53]
	v_mfma_f32_16x16x32_bf16 v[42:45], v[176:179], v[184:187], v[42:45]
	v_mfma_f32_16x16x32_bf16 v[34:37], v[168:171], v[192:195], v[34:37]
	v_mfma_f32_16x16x32_bf16 v[26:29], v[176:179], v[192:195], v[26:29]
	v_mfma_f32_16x16x32_bf16 v[18:21], v[168:171], v[200:203], v[18:21]
	v_mfma_f32_16x16x32_bf16 v[10:13], v[176:179], v[200:203], v[10:13]
	v_mfma_f32_16x16x32_bf16 v[6:9], v[168:171], v[208:211], v[6:9]
	v_mfma_f32_16x16x32_bf16 v[2:5], v[176:179], v[208:211], v[2:5]
	v_mfma_f32_16x16x32_bf16 v[50:53], v[172:175], v[188:191], v[50:53]
	v_mfma_f32_16x16x32_bf16 v[42:45], v[180:183], v[188:191], v[42:45]
	v_mfma_f32_16x16x32_bf16 v[34:37], v[172:175], v[196:199], v[34:37]
	v_mfma_f32_16x16x32_bf16 v[26:29], v[180:183], v[196:199], v[26:29]
	v_mfma_f32_16x16x32_bf16 v[18:21], v[172:175], v[204:207], v[18:21]
	v_mfma_f32_16x16x32_bf16 v[10:13], v[180:183], v[204:207], v[10:13]
	v_mfma_f32_16x16x32_bf16 v[6:9], v[172:175], v[212:215], v[6:9]
	v_mfma_f32_16x16x32_bf16 v[2:5], v[180:183], v[212:215], v[2:5]
	s_setprio 0
	s_add_i32 s60, s60, 2
	s_add_u32 s22, s22, 0x100
	s_addc_u32 s23, s23, 0
	s_add_u32 s56, s56, 0x100
	s_addc_u32 s57, s57, 0
	s_cmp_gt_u32 s60, 29
	s_barrier
	s_cbranch_scc0 .LBB0_412
	s_and_b64 vcc, exec, s[10:11]
	s_cbranch_vccz .LBB0_415
	s_barrier

; #define PG8_STAGE(bufoff, gbase, voff) do { _Pragma("unroll") for (int _i = 0; _i < 2; ++_i) \
;         __builtin_amdgcn_global_load_lds((const unsigned*)((const char*)(gbase) + (voff)[_i]), (PG8_LAS unsigned*)(lds + (bufoff) + ldsw + _i * 8192), 16, 0, 0); } while (0)
; #define PG8_LDA(dst, b, h) do { _Pragma("unroll") for (int m = 0; m < 4; ++m) _Pragma("unroll") for (int k = 0; k < 2; ++k) dst[m][k] = *(const PG8_LAS bf16x8*)(lds + PG8_SA(b, h) + aoff + m * 2048 + k * 1024); } while (0)
; #define PG8_LDB(dst, b, h) do { _Pragma("unroll") for (int n = 0; n < 2; ++n) _Pragma("unroll") for (int k = 0; k < 2; ++k) dst[n][k] = *(const PG8_LAS bf16x8*)(lds + PG8_SB(b, h) + boff + n * 2048 + k * 1024); } while (0)
; #define PG8_WAIT_V(n) asm volatile("s_waitcnt vmcnt(" #n ")" ::: "memory")
; #define PG8_WAIT_L(n) asm volatile("s_waitcnt lgkmcnt(" #n ")" ::: "memory")
; #define PG8_BAR __builtin_amdgcn_s_barrier()
; #define PG8_SCHED __builtin_amdgcn_sched_barrier(0)
; template <class Epi, class Sched, bool ALIGN_EPI = false, bool SP2 = false, bool FP8 = false>
; __device__ __forceinline__ void gemm_phase(PG8_LAS unsigned char* lds, const Gemm g, const Sched& S, const Epi& E) {
;     ...
;             PG8_LDB(B0, 0, 0); PG8_LDB(B1, 0, 1); PG8_SCHED; PG8_LDA(At, 0, 0); PG8_STAGE(PG8_SA(1, 1), a1 + hstep, voffA);
;             PG8_WAIT_V(8); PG8_WAIT_L(0); PG8_BAR; PG8_MMA(0, 0, At, B0); PG8_MMA(0, 1, At, B1); PG8_BAR; PG8_SCHED;
;             PG8_LDA(At, 0, 1); PG8_STAGE(PG8_SB(0, 0), b2, voffB); PG8_STAGE(PG8_SB(0, 1), b2 + hstep, voffB); PG8_STAGE(PG8_SA(0, 0), a2, voffA);
;             PG8_WAIT_V(8); PG8_WAIT_L(0); PG8_BAR; PG8_MMA(1, 0, At, B0); PG8_MMA(1, 1, At, B1); PG8_BAR; PG8_SCHED;
.LBB0_1006:
	ds_read_b128 v[130:133], v194
	ds_read_b128 v[134:137], v194 offset:1024
	ds_read_b128 v[138:141], v194 offset:2048
	ds_read_b128 v[142:145], v194 offset:3072
	ds_read_b128 v[146:149], v195
	ds_read_b128 v[150:153], v195 offset:1024
	ds_read_b128 v[170:173], v195 offset:2048
	ds_read_b128 v[174:177], v195 offset:3072
	s_add_u32 s24, s22, 0xfff80080
	s_addc_u32 s25, s23, -1
	s_cmp_eq_u32 s61, 28
	s_cselect_b32 s27, s15, s25
	s_cselect_b32 s26, s49, s24
	s_cselect_b32 s25, s13, s60
	s_cselect_b32 s24, s56, s57
	v_lshl_add_u64 v[190:191], s[22:23], 0, v[162:163]
	s_add_i32 m0, s21, 0xc000
	ds_read_b128 v[178:181], v196
	ds_read_b128 v[182:185], v196 offset:1024
	ds_read_b128 v[186:189], v196 offset:2048
	ds_read_b128 v[198:201], v196 offset:3072
	ds_read_b128 v[202:205], v196 offset:4096
	ds_read_b128 v[206:209], v196 offset:5120
	ds_read_b128 v[210:213], v196 offset:6144
	ds_read_b128 v[214:217], v196 offset:7168
	global_load_lds_dwordx4 v[190:191], off
	v_lshl_add_u64 v[190:191], s[22:23], 0, v[164:165]
	s_add_i32 m0, s21, 0xe000
	s_nop 0
	global_load_lds_dwordx4 v[190:191], off
	s_waitcnt vmcnt(8)
	s_waitcnt lgkmcnt(0)
	s_barrier
	s_setprio 1
	s_waitcnt lgkmcnt(0)
	v_mfma_f32_16x16x32_bf16 v[126:129], v[130:133], v[178:181], v[126:129]
	v_mfma_f32_16x16x32_bf16 v[122:125], v[138:141], v[178:181], v[122:125]
	v_mfma_f32_16x16x32_bf16 v[110:113], v[130:133], v[186:189], v[110:113]
	v_mfma_f32_16x16x32_bf16 v[106:109], v[138:141], v[186:189], v[106:109]
	v_mfma_f32_16x16x32_bf16 v[94:97], v[130:133], v[202:205], v[94:97]
	v_mfma_f32_16x16x32_bf16 v[90:93], v[138:141], v[202:205], v[90:93]
	v_mfma_f32_16x16x32_bf16 v[78:81], v[130:133], v[210:213], v[78:81]
	v_mfma_f32_16x16x32_bf16 v[74:77], v[138:141], v[210:213], v[74:77]
	v_mfma_f32_16x16x32_bf16 v[126:129], v[134:137], v[182:185], v[126:129]
	v_mfma_f32_16x16x32_bf16 v[122:125], v[142:145], v[182:185], v[122:125]
	v_mfma_f32_16x16x32_bf16 v[110:113], v[134:137], v[198:201], v[110:113]
	v_mfma_f32_16x16x32_bf16 v[106:109], v[142:145], v[198:201], v[106:109]
	v_mfma_f32_16x16x32_bf16 v[94:97], v[134:137], v[206:209], v[94:97]
	v_mfma_f32_16x16x32_bf16 v[90:93], v[142:145], v[206:209], v[90:93]
	v_mfma_f32_16x16x32_bf16 v[78:81], v[134:137], v[214:217], v[78:81]
	v_mfma_f32_16x16x32_bf16 v[74:77], v[142:145], v[214:217], v[74:77]
	s_setprio 0
	s_setprio 1
	v_mfma_f32_16x16x32_bf16 v[118:121], v[146:149], v[178:181], v[118:121]
	v_mfma_f32_16x16x32_bf16 v[114:117], v[170:173], v[178:181], v[114:117]
	v_mfma_f32_16x16x32_bf16 v[102:105], v[146:149], v[186:189], v[102:105]
	v_mfma_f32_16x16x32_bf16 v[98:101], v[170:173], v[186:189], v[98:101]
	v_mfma_f32_16x16x32_bf16 v[86:89], v[146:149], v[202:205], v[86:89]
	v_mfma_f32_16x16x32_bf16 v[82:85], v[170:173], v[202:205], v[82:85]
	v_mfma_f32_16x16x32_bf16 v[70:73], v[146:149], v[210:213], v[70:73]
	v_mfma_f32_16x16x32_bf16 v[66:69], v[170:173], v[210:213], v[66:69]
	v_mfma_f32_16x16x32_bf16 v[118:121], v[150:153], v[182:185], v[118:121]
	v_mfma_f32_16x16x32_bf16 v[114:117], v[174:177], v[182:185], v[114:117]
	v_mfma_f32_16x16x32_bf16 v[102:105], v[150:153], v[198:201], v[102:105]
	v_mfma_f32_16x16x32_bf16 v[98:101], v[174:177], v[198:201], v[98:101]
	v_mfma_f32_16x16x32_bf16 v[86:89], v[150:153], v[206:209], v[86:89]
	v_mfma_f32_16x16x32_bf16 v[82:85], v[174:177], v[206:209], v[82:85]
	v_mfma_f32_16x16x32_bf16 v[70:73], v[150:153], v[214:217], v[70:73]
	v_mfma_f32_16x16x32_bf16 v[66:69], v[174:177], v[214:217], v[66:69]
	s_setprio 0
	s_barrier
	s_add_i32 s62, s44, s33
	v_lshl_add_u64 v[190:191], s[24:25], 0, v[156:157]
	s_mov_b32 m0, s62
	ds_read_b128 v[178:181], v196 offset:16384
	ds_read_b128 v[182:185], v196 offset:17408
	ds_read_b128 v[186:189], v196 offset:18432
	ds_read_b128 v[198:201], v196 offset:19456
	ds_read_b128 v[202:205], v196 offset:20480
	ds_read_b128 v[206:209], v196 offset:21504
	ds_read_b128 v[210:213], v196 offset:22528
	ds_read_b128 v[214:217], v196 offset:23552
	global_load_lds_dwordx4 v[190:191], off
	s_add_i32 m0, s62, 0x2000
	s_add_u32 s62, s24, 0x80000
	v_lshl_add_u64 v[218:219], s[24:25], 0, v[160:161]
	s_addc_u32 s63, s25, 0
	s_add_i32 s68, s45, s33
	global_load_lds_dwordx4 v[218:219], off
	v_lshl_add_u64 v[220:221], s[62:63], 0, v[156:157]
	s_mov_b32 m0, s68
	v_lshl_add_u64 v[222:223], s[26:27], 0, v[158:159]
	global_load_lds_dwordx4 v[220:221], off
	v_lshl_add_u64 v[220:221], s[62:63], 0, v[160:161]
	s_add_i32 m0, s68, 0x2000
	s_nop 0
	global_load_lds_dwordx4 v[220:221], off
	v_lshl_add_u64 v[220:221], s[26:27], 0, v[154:155]
	s_mov_b32 m0, s21
	s_nop 0
	global_load_lds_dwordx4 v[220:221], off
	s_mov_b32 m0, s34
	s_nop 0
	global_load_lds_dwordx4 v[222:223], off
	s_waitcnt vmcnt(8)
	s_waitcnt lgkmcnt(0)
	s_barrier
; #define PG8_STAGE(bufoff, gbase, voff) do { _Pragma("unroll") for (int _i = 0; _i < 2; ++_i) \
;         __builtin_amdgcn_global_load_lds((const unsigned*)((const char*)(gbase) + (voff)[_i]), (PG8_LAS unsigned*)(lds + (bufoff) + ldsw + _i * 8192), 16, 0, 0); } while (0)
; #define PG8_LDA(dst, b, h) do { _Pragma("unroll") for (int m = 0; m < 4; ++m) _Pragma("unroll") for (int k = 0; k < 2; ++k) dst[m][k] = *(const PG8_LAS bf16x8*)(lds + PG8_SA(b, h) + aoff + m * 2048 + k * 1024); } while (0)
; #define PG8_LDB(dst, b, h) do { _Pragma("unroll") for (int n = 0; n < 2; ++n) _Pragma("unroll") for (int k = 0; k < 2; ++k) dst[n][k] = *(const PG8_LAS bf16x8*)(lds + PG8_SB(b, h) + boff + n * 2048 + k * 1024); } while (0)
; #define PG8_WAIT_V(n) asm volatile("s_waitcnt vmcnt(" #n ")" ::: "memory")
; #define PG8_WAIT_L(n) asm volatile("s_waitcnt lgkmcnt(" #n ")" ::: "memory")
; #define PG8_BAR __builtin_amdgcn_s_barrier()
; #define PG8_SCHED __builtin_amdgcn_sched_barrier(0)
; template <class Epi, class Sched, bool ALIGN_EPI = false, bool SP2 = false, bool FP8 = false>
; __device__ __forceinline__ void gemm_phase(PG8_LAS unsigned char* lds, const Gemm g, const Sched& S, const Epi& E) {
;     ...
;             PG8_WAIT_V(8); PG8_WAIT_L(0); PG8_BAR; PG8_MMA(1, 0, At, B0); PG8_MMA(1, 1, At, B1); PG8_BAR; PG8_SCHED;
;             PG8_LDB(B0, 1, 0); PG8_LDB(B1, 1, 1); PG8_SCHED; PG8_LDA(At, 1, 0); PG8_STAGE(PG8_SA(0, 1), a2 + hstep, voffA);
;             PG8_WAIT_V(8); PG8_WAIT_L(0); PG8_BAR; PG8_MMA(0, 0, At, B0); PG8_MMA(0, 1, At, B1); PG8_BAR; PG8_SCHED;
	s_setprio 1
	s_waitcnt lgkmcnt(0)
	v_mfma_f32_16x16x32_bf16 v[62:65], v[130:133], v[178:181], v[62:65]
	v_mfma_f32_16x16x32_bf16 v[58:61], v[138:141], v[178:181], v[58:61]
	v_mfma_f32_16x16x32_bf16 v[46:49], v[130:133], v[186:189], v[46:49]
	v_mfma_f32_16x16x32_bf16 v[42:45], v[138:141], v[186:189], v[42:45]
	v_mfma_f32_16x16x32_bf16 v[30:33], v[130:133], v[202:205], v[30:33]
	v_mfma_f32_16x16x32_bf16 v[26:29], v[138:141], v[202:205], v[26:29]
	v_mfma_f32_16x16x32_bf16 v[14:17], v[130:133], v[210:213], v[14:17]
	v_mfma_f32_16x16x32_bf16 v[10:13], v[138:141], v[210:213], v[10:13]
	v_mfma_f32_16x16x32_bf16 v[62:65], v[134:137], v[182:185], v[62:65]
	v_mfma_f32_16x16x32_bf16 v[58:61], v[142:145], v[182:185], v[58:61]
	v_mfma_f32_16x16x32_bf16 v[46:49], v[134:137], v[198:201], v[46:49]
	v_mfma_f32_16x16x32_bf16 v[42:45], v[142:145], v[198:201], v[42:45]
	v_mfma_f32_16x16x32_bf16 v[30:33], v[134:137], v[206:209], v[30:33]
	v_mfma_f32_16x16x32_bf16 v[26:29], v[142:145], v[206:209], v[26:29]
	v_mfma_f32_16x16x32_bf16 v[14:17], v[134:137], v[214:217], v[14:17]
	v_mfma_f32_16x16x32_bf16 v[10:13], v[142:145], v[214:217], v[10:13]
	s_setprio 0
	s_setprio 1
	v_mfma_f32_16x16x32_bf16 v[54:57], v[146:149], v[178:181], v[54:57]
	v_mfma_f32_16x16x32_bf16 v[50:53], v[170:173], v[178:181], v[50:53]
	v_mfma_f32_16x16x32_bf16 v[38:41], v[146:149], v[186:189], v[38:41]
	v_mfma_f32_16x16x32_bf16 v[34:37], v[170:173], v[186:189], v[34:37]
	v_mfma_f32_16x16x32_bf16 v[22:25], v[146:149], v[202:205], v[22:25]
	v_mfma_f32_16x16x32_bf16 v[18:21], v[170:173], v[202:205], v[18:21]
	v_mfma_f32_16x16x32_bf16 v[6:9], v[146:149], v[210:213], v[6:9]
	v_mfma_f32_16x16x32_bf16 v[2:5], v[170:173], v[210:213], v[2:5]
	v_mfma_f32_16x16x32_bf16 v[54:57], v[150:153], v[182:185], v[54:57]
	v_mfma_f32_16x16x32_bf16 v[50:53], v[174:177], v[182:185], v[50:53]
	v_mfma_f32_16x16x32_bf16 v[38:41], v[150:153], v[198:201], v[38:41]
	v_mfma_f32_16x16x32_bf16 v[34:37], v[174:177], v[198:201], v[34:37]
	v_mfma_f32_16x16x32_bf16 v[22:25], v[150:153], v[206:209], v[22:25]
	v_mfma_f32_16x16x32_bf16 v[18:21], v[174:177], v[206:209], v[18:21]
	v_mfma_f32_16x16x32_bf16 v[6:9], v[150:153], v[214:217], v[6:9]
	v_mfma_f32_16x16x32_bf16 v[2:5], v[174:177], v[214:217], v[2:5]
	s_setprio 0
	s_barrier
	s_add_i32 s62, 0, 0x18000
	s_add_i32 s63, 0, 0x1c000
	v_add_u32_e32 v142, s62, v192
	v_add_u32_e32 v174, s63, v192
	ds_read_b128 v[130:133], v142
	ds_read_b128 v[134:137], v142 offset:1024
	ds_read_b128 v[138:141], v142 offset:2048
	ds_read_b128 v[142:145], v142 offset:3072
	ds_read_b128 v[146:149], v174
	ds_read_b128 v[150:153], v174 offset:1024
	ds_read_b128 v[170:173], v174 offset:2048
	ds_read_b128 v[174:177], v174 offset:3072
	s_add_u32 s26, s26, 0x80000
	s_addc_u32 s27, s27, 0
	s_mov_b32 m0, s35
	v_lshl_add_u64 v[224:225], s[26:27], 0, v[154:155]
	ds_read_b128 v[178:181], v196 offset:32768
	ds_read_b128 v[182:185], v196 offset:33792
	ds_read_b128 v[186:189], v196 offset:34816
	ds_read_b128 v[198:201], v196 offset:35840
	ds_read_b128 v[202:205], v196 offset:36864
	ds_read_b128 v[206:209], v196 offset:37888
	ds_read_b128 v[210:213], v196 offset:38912
	ds_read_b128 v[214:217], v196 offset:39936
	global_load_lds_dwordx4 v[224:225], off
	v_lshl_add_u64 v[224:225], s[26:27], 0, v[158:159]
	s_mov_b32 m0, s36
	s_nop 0
	global_load_lds_dwordx4 v[224:225], off
	s_waitcnt vmcnt(8)
	s_waitcnt lgkmcnt(0)
	s_barrier
	s_setprio 1
	s_waitcnt lgkmcnt(0)
	v_mfma_f32_16x16x32_bf16 v[126:129], v[130:133], v[178:181], v[126:129]
	v_mfma_f32_16x16x32_bf16 v[122:125], v[138:141], v[178:181], v[122:125]
	v_mfma_f32_16x16x32_bf16 v[110:113], v[130:133], v[186:189], v[110:113]
	v_mfma_f32_16x16x32_bf16 v[106:109], v[138:141], v[186:189], v[106:109]
	v_mfma_f32_16x16x32_bf16 v[94:97], v[130:133], v[202:205], v[94:97]
	v_mfma_f32_16x16x32_bf16 v[90:93], v[138:141], v[202:205], v[90:93]
	v_mfma_f32_16x16x32_bf16 v[78:81], v[130:133], v[210:213], v[78:81]
	v_mfma_f32_16x16x32_bf16 v[74:77], v[138:141], v[210:213], v[74:77]
	v_mfma_f32_16x16x32_bf16 v[126:129], v[134:137], v[182:185], v[126:129]
	v_mfma_f32_16x16x32_bf16 v[122:125], v[142:145], v[182:185], v[122:125]
	v_mfma_f32_16x16x32_bf16 v[110:113], v[134:137], v[198:201], v[110:113]
	v_mfma_f32_16x16x32_bf16 v[106:109], v[142:145], v[198:201], v[106:109]
	v_mfma_f32_16x16x32_bf16 v[94:97], v[134:137], v[206:209], v[94:97]
	v_mfma_f32_16x16x32_bf16 v[90:93], v[142:145], v[206:209], v[90:93]
	v_mfma_f32_16x16x32_bf16 v[78:81], v[134:137], v[214:217], v[78:81]
	v_mfma_f32_16x16x32_bf16 v[74:77], v[142:145], v[214:217], v[74:77]
	s_setprio 0
	s_setprio 1
	v_mfma_f32_16x16x32_bf16 v[118:121], v[146:149], v[178:181], v[118:121]
	v_mfma_f32_16x16x32_bf16 v[114:117], v[170:173], v[178:181], v[114:117]
	v_mfma_f32_16x16x32_bf16 v[102:105], v[146:149], v[186:189], v[102:105]
	v_mfma_f32_16x16x32_bf16 v[98:101], v[170:173], v[186:189], v[98:101]
	v_mfma_f32_16x16x32_bf16 v[86:89], v[146:149], v[202:205], v[86:89]
	v_mfma_f32_16x16x32_bf16 v[82:85], v[170:173], v[202:205], v[82:85]
	v_mfma_f32_16x16x32_bf16 v[70:73], v[146:149], v[210:213], v[70:73]
	v_mfma_f32_16x16x32_bf16 v[66:69], v[170:173], v[210:213], v[66:69]
	v_mfma_f32_16x16x32_bf16 v[118:121], v[150:153], v[182:185], v[118:121]
	v_mfma_f32_16x16x32_bf16 v[114:117], v[174:177], v[182:185], v[114:117]
	v_mfma_f32_16x16x32_bf16 v[102:105], v[150:153], v[198:201], v[102:105]
	v_mfma_f32_16x16x32_bf16 v[98:101], v[174:177], v[198:201], v[98:101]
	v_mfma_f32_16x16x32_bf16 v[86:89], v[150:153], v[206:209], v[86:89]
	v_mfma_f32_16x16x32_bf16 v[82:85], v[174:177], v[206:209], v[82:85]
	v_mfma_f32_16x16x32_bf16 v[70:73], v[150:153], v[214:217], v[70:73]
	v_mfma_f32_16x16x32_bf16 v[66:69], v[174:177], v[214:217], v[66:69]
	s_setprio 0
	s_barrier
; #define PG8_STAGE(bufoff, gbase, voff) do { _Pragma("unroll") for (int _i = 0; _i < 2; ++_i) \
;         __builtin_amdgcn_global_load_lds((const unsigned*)((const char*)(gbase) + (voff)[_i]), (PG8_LAS unsigned*)(lds + (bufoff) + ldsw + _i * 8192), 16, 0, 0); } while (0)
; #define PG8_LDA(dst, b, h) do { _Pragma("unroll") for (int m = 0; m < 4; ++m) _Pragma("unroll") for (int k = 0; k < 2; ++k) dst[m][k] = *(const PG8_LAS bf16x8*)(lds + PG8_SA(b, h) + aoff + m * 2048 + k * 1024); } while (0)
; #define PG8_WAIT_V(n) asm volatile("s_waitcnt vmcnt(" #n ")" ::: "memory")
; #define PG8_WAIT_L(n) asm volatile("s_waitcnt lgkmcnt(" #n ")" ::: "memory")
; #define PG8_BAR __builtin_amdgcn_s_barrier()
; #define PG8_SCHED __builtin_amdgcn_sched_barrier(0)
; template <class Epi, class Sched, bool ALIGN_EPI = false, bool SP2 = false, bool FP8 = false>
; __device__ __forceinline__ void gemm_phase(PG8_LAS unsigned char* lds, const Gemm g, const Sched& S, const Epi& E) {
;     ...
;         for (int t = 0; t < nt; t += 2) {
;             const bool last = (t == nt - 2);
;             const char* a1 = cA + (size_t)(t + 1) * kstep;
;             const char* a2 = last ? nA : cA + (size_t)(t + 2) * kstep; const char* b2 = last ? nB : cB + (size_t)(t + 2) * kstep;
;     ...
;             PG8_LDA(At, 1, 1); PG8_STAGE(PG8_SB(1, 0), b3, voffB); PG8_STAGE(PG8_SB(1, 1), b3 + hstep, voffB); PG8_STAGE(PG8_SA(1, 0), a3, voffA);
;             PG8_WAIT_V(8); PG8_WAIT_L(0); PG8_BAR; PG8_MMA(1, 0, At, B0); PG8_MMA(1, 1, At, B1); PG8_BAR; PG8_SCHED;
	s_add_i32 s26, s62, s33
	v_lshl_add_u64 v[190:191], v[190:191], 0, s[4:5]
	s_mov_b32 m0, s26
	ds_read_b128 v[178:181], v196 offset:49152
	ds_read_b128 v[182:185], v196 offset:50176
	ds_read_b128 v[186:189], v196 offset:51200
	ds_read_b128 v[198:201], v196 offset:52224
	ds_read_b128 v[202:205], v196 offset:53248
	ds_read_b128 v[206:209], v196 offset:54272
	ds_read_b128 v[210:213], v196 offset:55296
	ds_read_b128 v[214:217], v196 offset:56320
	global_load_lds_dwordx4 v[190:191], off
	s_add_i32 m0, s26, 0x2000
	s_add_u32 s24, s24, 0x80080
	v_lshl_add_u64 v[190:191], v[218:219], 0, s[4:5]
	s_addc_u32 s25, s25, 0
	s_add_i32 s26, s63, s33
	global_load_lds_dwordx4 v[190:191], off
	v_lshl_add_u64 v[190:191], s[24:25], 0, v[156:157]
	s_mov_b32 m0, s26
	s_nop 0
	global_load_lds_dwordx4 v[190:191], off
	v_lshl_add_u64 v[190:191], s[24:25], 0, v[160:161]
	s_add_i32 m0, s26, 0x2000
	s_nop 0
	global_load_lds_dwordx4 v[190:191], off
	v_lshl_add_u64 v[190:191], v[220:221], 0, s[4:5]
	s_mov_b32 m0, s41
	s_nop 0
	global_load_lds_dwordx4 v[190:191], off
	v_lshl_add_u64 v[190:191], v[222:223], 0, s[4:5]
	s_mov_b32 m0, s42
	s_nop 0
	global_load_lds_dwordx4 v[190:191], off
	s_waitcnt vmcnt(8)
	s_waitcnt lgkmcnt(0)
	s_barrier
	s_setprio 1
	s_waitcnt lgkmcnt(0)
	v_mfma_f32_16x16x32_bf16 v[62:65], v[130:133], v[178:181], v[62:65]
	v_mfma_f32_16x16x32_bf16 v[58:61], v[138:141], v[178:181], v[58:61]
	v_mfma_f32_16x16x32_bf16 v[46:49], v[130:133], v[186:189], v[46:49]
	v_mfma_f32_16x16x32_bf16 v[42:45], v[138:141], v[186:189], v[42:45]
	v_mfma_f32_16x16x32_bf16 v[30:33], v[130:133], v[202:205], v[30:33]
	v_mfma_f32_16x16x32_bf16 v[26:29], v[138:141], v[202:205], v[26:29]
	v_mfma_f32_16x16x32_bf16 v[14:17], v[130:133], v[210:213], v[14:17]
	v_mfma_f32_16x16x32_bf16 v[10:13], v[138:141], v[210:213], v[10:13]
	v_mfma_f32_16x16x32_bf16 v[62:65], v[134:137], v[182:185], v[62:65]
	v_mfma_f32_16x16x32_bf16 v[58:61], v[142:145], v[182:185], v[58:61]
	v_mfma_f32_16x16x32_bf16 v[46:49], v[134:137], v[198:201], v[46:49]
	v_mfma_f32_16x16x32_bf16 v[42:45], v[142:145], v[198:201], v[42:45]
	v_mfma_f32_16x16x32_bf16 v[30:33], v[134:137], v[206:209], v[30:33]
	v_mfma_f32_16x16x32_bf16 v[26:29], v[142:145], v[206:209], v[26:29]
	v_mfma_f32_16x16x32_bf16 v[14:17], v[134:137], v[214:217], v[14:17]
	v_mfma_f32_16x16x32_bf16 v[10:13], v[142:145], v[214:217], v[10:13]
	s_setprio 0
	s_setprio 1
	v_mfma_f32_16x16x32_bf16 v[54:57], v[146:149], v[178:181], v[54:57]
	v_mfma_f32_16x16x32_bf16 v[50:53], v[170:173], v[178:181], v[50:53]
	v_mfma_f32_16x16x32_bf16 v[38:41], v[146:149], v[186:189], v[38:41]
	v_mfma_f32_16x16x32_bf16 v[34:37], v[170:173], v[186:189], v[34:37]
	v_mfma_f32_16x16x32_bf16 v[22:25], v[146:149], v[202:205], v[22:25]
	v_mfma_f32_16x16x32_bf16 v[18:21], v[170:173], v[202:205], v[18:21]
	v_mfma_f32_16x16x32_bf16 v[6:9], v[146:149], v[210:213], v[6:9]
	v_mfma_f32_16x16x32_bf16 v[2:5], v[170:173], v[210:213], v[2:5]
	v_mfma_f32_16x16x32_bf16 v[54:57], v[150:153], v[182:185], v[54:57]
	v_mfma_f32_16x16x32_bf16 v[50:53], v[174:177], v[182:185], v[50:53]
	v_mfma_f32_16x16x32_bf16 v[38:41], v[150:153], v[198:201], v[38:41]
	v_mfma_f32_16x16x32_bf16 v[34:37], v[174:177], v[198:201], v[34:37]
	v_mfma_f32_16x16x32_bf16 v[22:25], v[150:153], v[206:209], v[22:25]
	v_mfma_f32_16x16x32_bf16 v[18:21], v[174:177], v[206:209], v[18:21]
	v_mfma_f32_16x16x32_bf16 v[6:9], v[150:153], v[214:217], v[6:9]
	v_mfma_f32_16x16x32_bf16 v[2:5], v[174:177], v[214:217], v[2:5]
	s_setprio 0
	s_add_i32 s61, s61, 2
	s_add_u32 s22, s22, 0x100
	s_addc_u32 s23, s23, 0
	s_add_u32 s57, s57, 0x100
	s_addc_u32 s60, s60, 0
	s_cmp_gt_u32 s61, 29
	s_barrier
	s_cbranch_scc0 .LBB0_1006
	s_and_b64 vcc, exec, s[8:9]
	s_cbranch_vccz .LBB0_1009
	s_barrier

; #define PG8_STAGE(bufoff, gbase, voff) do { _Pragma("unroll") for (int _i = 0; _i < 2; ++_i) \
;         __builtin_amdgcn_global_load_lds((const unsigned*)((const char*)(gbase) + (voff)[_i]), (PG8_LAS unsigned*)(lds + (bufoff) + ldsw + _i * 8192), 16, 0, 0); } while (0)
; #define PG8_LDA(dst, b, h) do { _Pragma("unroll") for (int m = 0; m < 4; ++m) _Pragma("unroll") for (int k = 0; k < 2; ++k) dst[m][k] = *(const PG8_LAS bf16x8*)(lds + PG8_SA(b, h) + aoff + m * 2048 + k * 1024); } while (0)
; #define PG8_LDB(dst, b, h) do { _Pragma("unroll") for (int n = 0; n < 2; ++n) _Pragma("unroll") for (int k = 0; k < 2; ++k) dst[n][k] = *(const PG8_LAS bf16x8*)(lds + PG8_SB(b, h) + boff + n * 2048 + k * 1024); } while (0)
; #define PG8_WAIT_V(n) asm volatile("s_waitcnt vmcnt(" #n ")" ::: "memory")
; #define PG8_WAIT_L(n) asm volatile("s_waitcnt lgkmcnt(" #n ")" ::: "memory")
; #define PG8_BAR __builtin_amdgcn_s_barrier()
; #define PG8_SCHED __builtin_amdgcn_sched_barrier(0)
; template <class Epi, class Sched, bool ALIGN_EPI = false, bool SP2 = false, bool FP8 = false>
; __device__ __forceinline__ void gemm_phase(PG8_LAS unsigned char* lds, const Gemm g, const Sched& S, const Epi& E) {
;     ...
;             PG8_LDB(B0, 0, 0); PG8_LDB(B1, 0, 1); PG8_SCHED; PG8_LDA(At, 0, 0); PG8_STAGE(PG8_SA(1, 1), a1 + hstep, voffA);
;             PG8_WAIT_V(8); PG8_WAIT_L(0); PG8_BAR; PG8_MMA(0, 0, At, B0); PG8_MMA(0, 1, At, B1); PG8_BAR; PG8_SCHED;
;             PG8_LDA(At, 0, 1); PG8_STAGE(PG8_SB(0, 0), b2, voffB); PG8_STAGE(PG8_SB(0, 1), b2 + hstep, voffB); PG8_STAGE(PG8_SA(0, 0), a2, voffA);
;             PG8_WAIT_V(8); PG8_WAIT_L(0); PG8_BAR; PG8_MMA(1, 0, At, B0); PG8_MMA(1, 1, At, B1); PG8_BAR; PG8_SCHED;
.LBB0_1142:
	ds_read_b128 v[26:29], v188
	ds_read_b128 v[30:33], v188 offset:1024
	ds_read_b128 v[18:21], v188 offset:2048
	ds_read_b128 v[22:25], v188 offset:3072
	ds_read_b128 v[10:13], v189
	ds_read_b128 v[14:17], v189 offset:1024
	ds_read_b128 v[2:5], v189 offset:2048
	ds_read_b128 v[6:9], v189 offset:3072
	s_add_u32 s26, s24, 0xfffc0080
	s_addc_u32 s27, s25, -1
	s_cmp_eq_u32 s61, 12
	s_cselect_b32 s29, s17, s27
	s_cselect_b32 s28, s49, s26
	s_cselect_b32 s27, s15, s60
	s_cselect_b32 s26, s56, s57
	v_lshl_add_u64 v[216:217], s[24:25], 0, v[170:171]
	s_add_i32 m0, s23, 0xc000
	ds_read_b128 v[178:181], v190
	ds_read_b128 v[182:185], v190 offset:1024
	ds_read_b128 v[192:195], v190 offset:2048
	ds_read_b128 v[196:199], v190 offset:3072
	ds_read_b128 v[200:203], v190 offset:4096
	ds_read_b128 v[204:207], v190 offset:5120
	ds_read_b128 v[208:211], v190 offset:6144
	ds_read_b128 v[212:215], v190 offset:7168
	global_load_lds_dwordx4 v[216:217], off
	v_lshl_add_u64 v[216:217], s[24:25], 0, v[172:173]
	s_add_i32 m0, s23, 0xe000
	s_nop 0
	global_load_lds_dwordx4 v[216:217], off
	s_waitcnt vmcnt(8)
	s_waitcnt lgkmcnt(0)
	s_barrier
	s_setprio 1
	s_waitcnt lgkmcnt(0)
	v_mfma_f32_16x16x128_f8f6f4 v[158:161], v[26:33], v[178:185], v[158:161]
	v_mfma_f32_16x16x128_f8f6f4 v[150:153], v[18:25], v[178:185], v[150:153]
	v_mfma_f32_16x16x128_f8f6f4 v[142:145], v[26:33], v[192:199], v[142:145]
	v_mfma_f32_16x16x128_f8f6f4 v[134:137], v[18:25], v[192:199], v[134:137]
	v_mfma_f32_16x16x128_f8f6f4 v[126:129], v[26:33], v[200:207], v[126:129]
	v_mfma_f32_16x16x128_f8f6f4 v[118:121], v[18:25], v[200:207], v[118:121]
	v_mfma_f32_16x16x128_f8f6f4 v[110:113], v[26:33], v[208:215], v[110:113]
	v_mfma_f32_16x16x128_f8f6f4 v[102:105], v[18:25], v[208:215], v[102:105]
	s_setprio 0
	s_setprio 1
	v_mfma_f32_16x16x128_f8f6f4 v[154:157], v[10:17], v[178:185], v[154:157]
	v_mfma_f32_16x16x128_f8f6f4 v[146:149], v[2:9], v[178:185], v[146:149]
	v_mfma_f32_16x16x128_f8f6f4 v[138:141], v[10:17], v[192:199], v[138:141]
	v_mfma_f32_16x16x128_f8f6f4 v[130:133], v[2:9], v[192:199], v[130:133]
	v_mfma_f32_16x16x128_f8f6f4 v[122:125], v[10:17], v[200:207], v[122:125]
	v_mfma_f32_16x16x128_f8f6f4 v[114:117], v[2:9], v[200:207], v[114:117]
	v_mfma_f32_16x16x128_f8f6f4 v[106:109], v[10:17], v[208:215], v[106:109]
	v_mfma_f32_16x16x128_f8f6f4 v[98:101], v[2:9], v[208:215], v[98:101]
	s_setprio 0
	s_barrier
	s_add_i32 s62, s45, s34
	v_lshl_add_u64 v[178:179], s[26:27], 0, v[166:167]
	s_mov_b32 m0, s62
	ds_read_b128 v[192:195], v190 offset:16384
	ds_read_b128 v[196:199], v190 offset:17408
	ds_read_b128 v[200:203], v190 offset:18432
	ds_read_b128 v[204:207], v190 offset:19456
	ds_read_b128 v[208:211], v190 offset:20480
	ds_read_b128 v[212:215], v190 offset:21504
	ds_read_b128 v[216:219], v190 offset:22528
	ds_read_b128 v[220:223], v190 offset:23552
	global_load_lds_dwordx4 v[178:179], off
	s_add_i32 m0, s62, 0x2000
	s_add_u32 s62, s26, 0x40000
	v_lshl_add_u64 v[180:181], s[26:27], 0, v[162:163]
	s_addc_u32 s63, s27, 0
	s_add_i32 s68, s46, s34
	global_load_lds_dwordx4 v[180:181], off
	v_lshl_add_u64 v[182:183], s[62:63], 0, v[166:167]
	s_mov_b32 m0, s68
	v_lshl_add_u64 v[184:185], s[28:29], 0, v[164:165]
	global_load_lds_dwordx4 v[182:183], off
	v_lshl_add_u64 v[182:183], s[62:63], 0, v[162:163]
	s_add_i32 m0, s68, 0x2000
	s_nop 0
	global_load_lds_dwordx4 v[182:183], off
	v_lshl_add_u64 v[182:183], s[28:29], 0, v[168:169]
	s_mov_b32 m0, s23
	s_nop 0
	global_load_lds_dwordx4 v[182:183], off
	s_mov_b32 m0, s37
	s_nop 0
	global_load_lds_dwordx4 v[184:185], off
	s_waitcnt vmcnt(8)
	s_waitcnt lgkmcnt(0)
	s_barrier
	s_setprio 1
	s_waitcnt lgkmcnt(0)
	v_mfma_f32_16x16x128_f8f6f4 v[94:97], v[26:33], v[192:199], v[94:97]
	v_mfma_f32_16x16x128_f8f6f4 v[86:89], v[18:25], v[192:199], v[86:89]
	v_mfma_f32_16x16x128_f8f6f4 v[78:81], v[26:33], v[200:207], v[78:81]
	v_mfma_f32_16x16x128_f8f6f4 v[70:73], v[18:25], v[200:207], v[70:73]
	v_mfma_f32_16x16x128_f8f6f4 v[62:65], v[26:33], v[208:215], v[62:65]
	v_mfma_f32_16x16x128_f8f6f4 v[54:57], v[18:25], v[208:215], v[54:57]
	v_mfma_f32_16x16x128_f8f6f4 v[46:49], v[26:33], v[216:223], v[46:49]
	v_mfma_f32_16x16x128_f8f6f4 v[38:41], v[18:25], v[216:223], v[38:41]
	s_setprio 0
	s_setprio 1
	v_mfma_f32_16x16x128_f8f6f4 v[90:93], v[10:17], v[192:199], v[90:93]
	v_mfma_f32_16x16x128_f8f6f4 v[82:85], v[2:9], v[192:199], v[82:85]
	v_mfma_f32_16x16x128_f8f6f4 v[74:77], v[10:17], v[200:207], v[74:77]
	v_mfma_f32_16x16x128_f8f6f4 v[66:69], v[2:9], v[200:207], v[66:69]
	v_mfma_f32_16x16x128_f8f6f4 v[58:61], v[10:17], v[208:215], v[58:61]
	v_mfma_f32_16x16x128_f8f6f4 v[50:53], v[2:9], v[208:215], v[50:53]
	v_mfma_f32_16x16x128_f8f6f4 v[42:45], v[10:17], v[216:223], v[42:45]
	v_mfma_f32_16x16x128_f8f6f4 v[34:37], v[2:9], v[216:223], v[34:37]
	s_setprio 0
	s_barrier
; #define PG8_STAGE(bufoff, gbase, voff) do { _Pragma("unroll") for (int _i = 0; _i < 2; ++_i) \
;         __builtin_amdgcn_global_load_lds((const unsigned*)((const char*)(gbase) + (voff)[_i]), (PG8_LAS unsigned*)(lds + (bufoff) + ldsw + _i * 8192), 16, 0, 0); } while (0)
; #define PG8_LDA(dst, b, h) do { _Pragma("unroll") for (int m = 0; m < 4; ++m) _Pragma("unroll") for (int k = 0; k < 2; ++k) dst[m][k] = *(const PG8_LAS bf16x8*)(lds + PG8_SA(b, h) + aoff + m * 2048 + k * 1024); } while (0)
; #define PG8_LDB(dst, b, h) do { _Pragma("unroll") for (int n = 0; n < 2; ++n) _Pragma("unroll") for (int k = 0; k < 2; ++k) dst[n][k] = *(const PG8_LAS bf16x8*)(lds + PG8_SB(b, h) + boff + n * 2048 + k * 1024); } while (0)
; #define PG8_WAIT_V(n) asm volatile("s_waitcnt vmcnt(" #n ")" ::: "memory")
; #define PG8_WAIT_L(n) asm volatile("s_waitcnt lgkmcnt(" #n ")" ::: "memory")
; #define PG8_BAR __builtin_amdgcn_s_barrier()
; #define PG8_SCHED __builtin_amdgcn_sched_barrier(0)
; template <class Epi, class Sched, bool ALIGN_EPI = false, bool SP2 = false, bool FP8 = false>
; __device__ __forceinline__ void gemm_phase(PG8_LAS unsigned char* lds, const Gemm g, const Sched& S, const Epi& E) {
;     ...
;         for (int t = 0; t < nt; t += 2) {
;             const bool last = (t == nt - 2);
;             const char* a1 = cA + (size_t)(t + 1) * kstep;
;             const char* a2 = last ? nA : cA + (size_t)(t + 2) * kstep; const char* b2 = last ? nB : cB + (size_t)(t + 2) * kstep;
;     ...
;             PG8_LDB(B0, 1, 0); PG8_LDB(B1, 1, 1); PG8_SCHED; PG8_LDA(At, 1, 0); PG8_STAGE(PG8_SA(0, 1), a2 + hstep, voffA);
;             PG8_WAIT_V(8); PG8_WAIT_L(0); PG8_BAR; PG8_MMA(0, 0, At, B0); PG8_MMA(0, 1, At, B1); PG8_BAR; PG8_SCHED;
;             PG8_LDA(At, 1, 1); PG8_STAGE(PG8_SB(1, 0), b3, voffB); PG8_STAGE(PG8_SB(1, 1), b3 + hstep, voffB); PG8_STAGE(PG8_SA(1, 0), a3, voffA);
;             PG8_WAIT_V(8); PG8_WAIT_L(0); PG8_BAR; PG8_MMA(1, 0, At, B0); PG8_MMA(1, 1, At, B1); PG8_BAR; PG8_SCHED;
;     ...
;         if constexpr (FP8) asm volatile("s_nop 15\n\ts_nop 15\n\ts_nop 15\n\ts_nop 15" ::: "memory");
	s_add_i32 s62, 0, 0x18000
	s_add_i32 s63, 0, 0x1c000
	v_add_u32_e32 v14, s62, v186
	v_add_u32_e32 v30, s63, v186
	ds_read_b128 v[2:5], v14
	ds_read_b128 v[6:9], v14 offset:1024
	ds_read_b128 v[10:13], v14 offset:2048
	ds_read_b128 v[14:17], v14 offset:3072
	ds_read_b128 v[18:21], v30
	ds_read_b128 v[22:25], v30 offset:1024
	ds_read_b128 v[26:29], v30 offset:2048
	ds_read_b128 v[30:33], v30 offset:3072
	s_add_u32 s28, s28, 0x40000
	s_addc_u32 s29, s29, 0
	s_mov_b32 m0, s38
	v_lshl_add_u64 v[224:225], s[28:29], 0, v[168:169]
	ds_read_b128 v[192:195], v190 offset:32768
	ds_read_b128 v[196:199], v190 offset:33792
	ds_read_b128 v[200:203], v190 offset:34816
	ds_read_b128 v[204:207], v190 offset:35840
	ds_read_b128 v[208:211], v190 offset:36864
	ds_read_b128 v[212:215], v190 offset:37888
	ds_read_b128 v[216:219], v190 offset:38912
	ds_read_b128 v[220:223], v190 offset:39936
	global_load_lds_dwordx4 v[224:225], off
	v_lshl_add_u64 v[224:225], s[28:29], 0, v[164:165]
	s_mov_b32 m0, s39
	s_nop 0
	global_load_lds_dwordx4 v[224:225], off
	s_waitcnt vmcnt(8)
	s_waitcnt lgkmcnt(0)
	s_barrier
	s_setprio 1
	s_waitcnt lgkmcnt(0)
	v_mfma_f32_16x16x128_f8f6f4 v[158:161], v[2:9], v[192:199], v[158:161]
	v_mfma_f32_16x16x128_f8f6f4 v[150:153], v[10:17], v[192:199], v[150:153]
	v_mfma_f32_16x16x128_f8f6f4 v[142:145], v[2:9], v[200:207], v[142:145]
	v_mfma_f32_16x16x128_f8f6f4 v[134:137], v[10:17], v[200:207], v[134:137]
	v_mfma_f32_16x16x128_f8f6f4 v[126:129], v[2:9], v[208:215], v[126:129]
	v_mfma_f32_16x16x128_f8f6f4 v[118:121], v[10:17], v[208:215], v[118:121]
	v_mfma_f32_16x16x128_f8f6f4 v[110:113], v[2:9], v[216:223], v[110:113]
	v_mfma_f32_16x16x128_f8f6f4 v[102:105], v[10:17], v[216:223], v[102:105]
	s_setprio 0
	s_setprio 1
	v_mfma_f32_16x16x128_f8f6f4 v[154:157], v[18:25], v[192:199], v[154:157]
	v_mfma_f32_16x16x128_f8f6f4 v[146:149], v[26:33], v[192:199], v[146:149]
	v_mfma_f32_16x16x128_f8f6f4 v[138:141], v[18:25], v[200:207], v[138:141]
	v_mfma_f32_16x16x128_f8f6f4 v[130:133], v[26:33], v[200:207], v[130:133]
	v_mfma_f32_16x16x128_f8f6f4 v[122:125], v[18:25], v[208:215], v[122:125]
	v_mfma_f32_16x16x128_f8f6f4 v[114:117], v[26:33], v[208:215], v[114:117]
	v_mfma_f32_16x16x128_f8f6f4 v[106:109], v[18:25], v[216:223], v[106:109]
	v_mfma_f32_16x16x128_f8f6f4 v[98:101], v[26:33], v[216:223], v[98:101]
	s_setprio 0
	s_barrier
	s_add_i32 s28, s62, s34
	v_lshl_add_u64 v[178:179], v[178:179], 0, s[8:9]
	s_mov_b32 m0, s28
	ds_read_b128 v[192:195], v190 offset:49152
	ds_read_b128 v[196:199], v190 offset:50176
	ds_read_b128 v[200:203], v190 offset:51200
	ds_read_b128 v[204:207], v190 offset:52224
	ds_read_b128 v[208:211], v190 offset:53248
	ds_read_b128 v[212:215], v190 offset:54272
	ds_read_b128 v[216:219], v190 offset:55296
	ds_read_b128 v[220:223], v190 offset:56320
	global_load_lds_dwordx4 v[178:179], off
	s_add_i32 m0, s28, 0x2000
	s_add_u32 s26, s26, 0x40080
	v_lshl_add_u64 v[178:179], v[180:181], 0, s[8:9]
	s_addc_u32 s27, s27, 0
	s_add_i32 s28, s63, s34
	global_load_lds_dwordx4 v[178:179], off
	v_lshl_add_u64 v[178:179], s[26:27], 0, v[166:167]
	s_mov_b32 m0, s28
	s_nop 0
	global_load_lds_dwordx4 v[178:179], off
	v_lshl_add_u64 v[178:179], s[26:27], 0, v[162:163]
	s_add_i32 m0, s28, 0x2000
	s_nop 0
	global_load_lds_dwordx4 v[178:179], off
	v_lshl_add_u64 v[178:179], v[182:183], 0, s[8:9]
	s_mov_b32 m0, s42
	s_nop 0
	global_load_lds_dwordx4 v[178:179], off
	v_lshl_add_u64 v[178:179], v[184:185], 0, s[8:9]
	s_mov_b32 m0, s43
	s_nop 0
	global_load_lds_dwordx4 v[178:179], off
	s_waitcnt vmcnt(8)
	s_waitcnt lgkmcnt(0)
	s_barrier
	s_setprio 1
	s_waitcnt lgkmcnt(0)
	v_mfma_f32_16x16x128_f8f6f4 v[94:97], v[2:9], v[192:199], v[94:97]
	v_mfma_f32_16x16x128_f8f6f4 v[86:89], v[10:17], v[192:199], v[86:89]
	v_mfma_f32_16x16x128_f8f6f4 v[78:81], v[2:9], v[200:207], v[78:81]
	v_mfma_f32_16x16x128_f8f6f4 v[70:73], v[10:17], v[200:207], v[70:73]
	v_mfma_f32_16x16x128_f8f6f4 v[62:65], v[2:9], v[208:215], v[62:65]
	v_mfma_f32_16x16x128_f8f6f4 v[54:57], v[10:17], v[208:215], v[54:57]
	v_mfma_f32_16x16x128_f8f6f4 v[46:49], v[2:9], v[216:223], v[46:49]
	v_mfma_f32_16x16x128_f8f6f4 v[38:41], v[10:17], v[216:223], v[38:41]
	s_setprio 0
	s_setprio 1
	v_mfma_f32_16x16x128_f8f6f4 v[90:93], v[18:25], v[192:199], v[90:93]
	v_mfma_f32_16x16x128_f8f6f4 v[82:85], v[26:33], v[192:199], v[82:85]
	v_mfma_f32_16x16x128_f8f6f4 v[74:77], v[18:25], v[200:207], v[74:77]
	v_mfma_f32_16x16x128_f8f6f4 v[66:69], v[26:33], v[200:207], v[66:69]
	v_mfma_f32_16x16x128_f8f6f4 v[58:61], v[18:25], v[208:215], v[58:61]
	v_mfma_f32_16x16x128_f8f6f4 v[50:53], v[26:33], v[208:215], v[50:53]
	v_mfma_f32_16x16x128_f8f6f4 v[42:45], v[18:25], v[216:223], v[42:45]
	v_mfma_f32_16x16x128_f8f6f4 v[34:37], v[26:33], v[216:223], v[34:37]
	s_setprio 0
	s_add_i32 s61, s61, 2
	s_add_u32 s24, s24, 0x100
	s_addc_u32 s25, s25, 0
	s_add_u32 s57, s57, 0x100
	s_addc_u32 s60, s60, 0
	s_cmp_gt_u32 s61, 13
	s_barrier
	s_cbranch_scc0 .LBB0_1142
	s_nop 15
	s_nop 15
	s_nop 15
	s_nop 15
	s_and_b64 vcc, exec, s[10:11]
	s_cbranch_vccz .LBB0_1145
	s_barrier

; #define PG8_STAGE(bufoff, gbase, voff) do { _Pragma("unroll") for (int _i = 0; _i < 2; ++_i) \
;         __builtin_amdgcn_global_load_lds((const unsigned*)((const char*)(gbase) + (voff)[_i]), (PG8_LAS unsigned*)(lds + (bufoff) + ldsw + _i * 8192), 16, 0, 0); } while (0)
; #define PG8_LDA(dst, b, h) do { _Pragma("unroll") for (int m = 0; m < 4; ++m) _Pragma("unroll") for (int k = 0; k < 2; ++k) dst[m][k] = *(const PG8_LAS bf16x8*)(lds + PG8_SA(b, h) + aoff + m * 2048 + k * 1024); } while (0)
; #define PG8_LDB(dst, b, h) do { _Pragma("unroll") for (int n = 0; n < 2; ++n) _Pragma("unroll") for (int k = 0; k < 2; ++k) dst[n][k] = *(const PG8_LAS bf16x8*)(lds + PG8_SB(b, h) + boff + n * 2048 + k * 1024); } while (0)
; #define PG8_WAIT_V(n) asm volatile("s_waitcnt vmcnt(" #n ")" ::: "memory")
; #define PG8_WAIT_L(n) asm volatile("s_waitcnt lgkmcnt(" #n ")" ::: "memory")
; #define PG8_BAR __builtin_amdgcn_s_barrier()
; #define PG8_SCHED __builtin_amdgcn_sched_barrier(0)
; template <class Epi, class Sched, bool ALIGN_EPI = false, bool SP2 = false, bool FP8 = false>
; __device__ __forceinline__ void gemm_phase(PG8_LAS unsigned char* lds, const Gemm g, const Sched& S, const Epi& E) {
;     ...
;             PG8_LDB(B0, 0, 0); PG8_LDB(B1, 0, 1); PG8_SCHED; PG8_LDA(At, 0, 0); PG8_STAGE(PG8_SA(1, 1), a1 + hstep, voffA);
;             PG8_WAIT_V(8); PG8_WAIT_L(0); PG8_BAR; PG8_MMA(0, 0, At, B0); PG8_MMA(0, 1, At, B1); PG8_BAR; PG8_SCHED;
;             PG8_LDA(At, 0, 1); PG8_STAGE(PG8_SB(0, 0), b2, voffB); PG8_STAGE(PG8_SB(0, 1), b2 + hstep, voffB); PG8_STAGE(PG8_SA(0, 0), a2, voffA);
;             PG8_WAIT_V(8); PG8_WAIT_L(0); PG8_BAR; PG8_MMA(1, 0, At, B0); PG8_MMA(1, 1, At, B1); PG8_BAR; PG8_SCHED;
.LBB0_1225:
	ds_read_b128 v[26:29], v190
	ds_read_b128 v[30:33], v190 offset:1024
	ds_read_b128 v[18:21], v190 offset:2048
	ds_read_b128 v[22:25], v190 offset:3072
	ds_read_b128 v[10:13], v191
	ds_read_b128 v[14:17], v191 offset:1024
	ds_read_b128 v[2:5], v191 offset:2048
	ds_read_b128 v[6:9], v191 offset:3072
	s_add_u32 s30, s28, 0xfff50080
	s_addc_u32 s31, s29, -1
	s_cmp_eq_u32 s72, 40
	s_cselect_b32 s35, s9, s31
	s_cselect_b32 s34, s8, s30
	s_cselect_b32 s31, s27, s71
	s_cselect_b32 s30, s26, s70
	v_lshl_add_u64 v[186:187], s[28:29], 0, v[170:171]
	s_add_i32 m0, s39, 0xc000
	ds_read_b128 v[178:181], v192
	ds_read_b128 v[182:185], v192 offset:1024
	ds_read_b128 v[194:197], v192 offset:2048
	ds_read_b128 v[198:201], v192 offset:3072
	ds_read_b128 v[202:205], v192 offset:4096
	ds_read_b128 v[206:209], v192 offset:5120
	ds_read_b128 v[210:213], v192 offset:6144
	ds_read_b128 v[214:217], v192 offset:7168
	global_load_lds_dwordx4 v[186:187], off
	v_lshl_add_u64 v[186:187], s[28:29], 0, v[172:173]
	s_add_i32 m0, s39, 0xe000
	s_nop 0
	global_load_lds_dwordx4 v[186:187], off
	s_waitcnt vmcnt(8)
	s_waitcnt lgkmcnt(0)
	s_barrier
	s_setprio 1
	s_waitcnt lgkmcnt(0)
	v_mfma_f32_16x16x128_f8f6f4 v[158:161], v[26:33], v[178:185], v[158:161]
	v_mfma_f32_16x16x128_f8f6f4 v[154:157], v[18:25], v[178:185], v[154:157]
	v_mfma_f32_16x16x128_f8f6f4 v[142:145], v[26:33], v[194:201], v[142:145]
	v_mfma_f32_16x16x128_f8f6f4 v[138:141], v[18:25], v[194:201], v[138:141]
	v_mfma_f32_16x16x128_f8f6f4 v[126:129], v[26:33], v[202:209], v[126:129]
	v_mfma_f32_16x16x128_f8f6f4 v[122:125], v[18:25], v[202:209], v[122:125]
	v_mfma_f32_16x16x128_f8f6f4 v[110:113], v[26:33], v[210:217], v[110:113]
	v_mfma_f32_16x16x128_f8f6f4 v[106:109], v[18:25], v[210:217], v[106:109]
	s_setprio 0
	s_setprio 1
	v_mfma_f32_16x16x128_f8f6f4 v[150:153], v[10:17], v[178:185], v[150:153]
	v_mfma_f32_16x16x128_f8f6f4 v[146:149], v[2:9], v[178:185], v[146:149]
	v_mfma_f32_16x16x128_f8f6f4 v[134:137], v[10:17], v[194:201], v[134:137]
	v_mfma_f32_16x16x128_f8f6f4 v[130:133], v[2:9], v[194:201], v[130:133]
	v_mfma_f32_16x16x128_f8f6f4 v[118:121], v[10:17], v[202:209], v[118:121]
	v_mfma_f32_16x16x128_f8f6f4 v[114:117], v[2:9], v[202:209], v[114:117]
	v_mfma_f32_16x16x128_f8f6f4 v[102:105], v[10:17], v[210:217], v[102:105]
	v_mfma_f32_16x16x128_f8f6f4 v[98:101], v[2:9], v[210:217], v[98:101]
	s_setprio 0
	s_barrier
	s_add_i32 s73, s56, s38
	v_lshl_add_u64 v[178:179], s[30:31], 0, v[164:165]
	s_mov_b32 m0, s73
	ds_read_b128 v[194:197], v192 offset:16384
	ds_read_b128 v[198:201], v192 offset:17408
	ds_read_b128 v[202:205], v192 offset:18432
	ds_read_b128 v[206:209], v192 offset:19456
	ds_read_b128 v[210:213], v192 offset:20480
	ds_read_b128 v[214:217], v192 offset:21504
	ds_read_b128 v[218:221], v192 offset:22528
	ds_read_b128 v[222:225], v192 offset:23552
	global_load_lds_dwordx4 v[178:179], off
	s_add_i32 m0, s73, 0x2000
	s_add_u32 s74, s30, 0xb0000
	v_lshl_add_u64 v[180:181], s[30:31], 0, v[168:169]
	s_addc_u32 s75, s31, 0
	s_add_i32 s73, s57, s38
	global_load_lds_dwordx4 v[180:181], off
	v_lshl_add_u64 v[182:183], s[74:75], 0, v[164:165]
	s_mov_b32 m0, s73
	v_lshl_add_u64 v[184:185], s[34:35], 0, v[166:167]
	global_load_lds_dwordx4 v[182:183], off
	v_lshl_add_u64 v[182:183], s[74:75], 0, v[168:169]
	s_add_i32 m0, s73, 0x2000
	s_nop 0
	global_load_lds_dwordx4 v[182:183], off
	v_lshl_add_u64 v[182:183], s[34:35], 0, v[162:163]
	s_mov_b32 m0, s39
	s_nop 0
	global_load_lds_dwordx4 v[182:183], off
	s_mov_b32 m0, s40
	s_nop 0
	global_load_lds_dwordx4 v[184:185], off
	s_waitcnt vmcnt(8)
	s_waitcnt lgkmcnt(0)
	s_barrier
	s_setprio 1
	s_waitcnt lgkmcnt(0)
	v_mfma_f32_16x16x128_f8f6f4 v[94:97], v[26:33], v[194:201], v[94:97]
	v_mfma_f32_16x16x128_f8f6f4 v[90:93], v[18:25], v[194:201], v[90:93]
	v_mfma_f32_16x16x128_f8f6f4 v[78:81], v[26:33], v[202:209], v[78:81]
	v_mfma_f32_16x16x128_f8f6f4 v[74:77], v[18:25], v[202:209], v[74:77]
	v_mfma_f32_16x16x128_f8f6f4 v[62:65], v[26:33], v[210:217], v[62:65]
	v_mfma_f32_16x16x128_f8f6f4 v[58:61], v[18:25], v[210:217], v[58:61]
	v_mfma_f32_16x16x128_f8f6f4 v[46:49], v[26:33], v[218:225], v[46:49]
	v_mfma_f32_16x16x128_f8f6f4 v[42:45], v[18:25], v[218:225], v[42:45]
	s_setprio 0
	s_setprio 1
	v_mfma_f32_16x16x128_f8f6f4 v[86:89], v[10:17], v[194:201], v[86:89]
	v_mfma_f32_16x16x128_f8f6f4 v[82:85], v[2:9], v[194:201], v[82:85]
	v_mfma_f32_16x16x128_f8f6f4 v[70:73], v[10:17], v[202:209], v[70:73]
	v_mfma_f32_16x16x128_f8f6f4 v[66:69], v[2:9], v[202:209], v[66:69]
	v_mfma_f32_16x16x128_f8f6f4 v[54:57], v[10:17], v[210:217], v[54:57]
	v_mfma_f32_16x16x128_f8f6f4 v[50:53], v[2:9], v[210:217], v[50:53]
	v_mfma_f32_16x16x128_f8f6f4 v[38:41], v[10:17], v[218:225], v[38:41]
	v_mfma_f32_16x16x128_f8f6f4 v[34:37], v[2:9], v[218:225], v[34:37]
	s_setprio 0
	s_barrier
; #define PG8_STAGE(bufoff, gbase, voff) do { _Pragma("unroll") for (int _i = 0; _i < 2; ++_i) \
;         __builtin_amdgcn_global_load_lds((const unsigned*)((const char*)(gbase) + (voff)[_i]), (PG8_LAS unsigned*)(lds + (bufoff) + ldsw + _i * 8192), 16, 0, 0); } while (0)
; #define PG8_LDA(dst, b, h) do { _Pragma("unroll") for (int m = 0; m < 4; ++m) _Pragma("unroll") for (int k = 0; k < 2; ++k) dst[m][k] = *(const PG8_LAS bf16x8*)(lds + PG8_SA(b, h) + aoff + m * 2048 + k * 1024); } while (0)
; #define PG8_LDB(dst, b, h) do { _Pragma("unroll") for (int n = 0; n < 2; ++n) _Pragma("unroll") for (int k = 0; k < 2; ++k) dst[n][k] = *(const PG8_LAS bf16x8*)(lds + PG8_SB(b, h) + boff + n * 2048 + k * 1024); } while (0)
; #define PG8_WAIT_V(n) asm volatile("s_waitcnt vmcnt(" #n ")" ::: "memory")
; #define PG8_WAIT_L(n) asm volatile("s_waitcnt lgkmcnt(" #n ")" ::: "memory")
; #define PG8_BAR __builtin_amdgcn_s_barrier()
; #define PG8_SCHED __builtin_amdgcn_sched_barrier(0)
; template <class Epi, class Sched, bool ALIGN_EPI = false, bool SP2 = false, bool FP8 = false>
; __device__ __forceinline__ void gemm_phase(PG8_LAS unsigned char* lds, const Gemm g, const Sched& S, const Epi& E) {
;     ...
;         for (int t = 0; t < nt; t += 2) {
;             const bool last = (t == nt - 2);
;             const char* a1 = cA + (size_t)(t + 1) * kstep;
;             const char* a2 = last ? nA : cA + (size_t)(t + 2) * kstep; const char* b2 = last ? nB : cB + (size_t)(t + 2) * kstep;
;     ...
;             PG8_LDB(B0, 1, 0); PG8_LDB(B1, 1, 1); PG8_SCHED; PG8_LDA(At, 1, 0); PG8_STAGE(PG8_SA(0, 1), a2 + hstep, voffA);
;             PG8_WAIT_V(8); PG8_WAIT_L(0); PG8_BAR; PG8_MMA(0, 0, At, B0); PG8_MMA(0, 1, At, B1); PG8_BAR; PG8_SCHED;
;             PG8_LDA(At, 1, 1); PG8_STAGE(PG8_SB(1, 0), b3, voffB); PG8_STAGE(PG8_SB(1, 1), b3 + hstep, voffB); PG8_STAGE(PG8_SA(1, 0), a3, voffA);
;             PG8_WAIT_V(8); PG8_WAIT_L(0); PG8_BAR; PG8_MMA(1, 0, At, B0); PG8_MMA(1, 1, At, B1); PG8_BAR; PG8_SCHED;
;     ...
;         if constexpr (FP8) asm volatile("s_nop 15\n\ts_nop 15\n\ts_nop 15\n\ts_nop 15" ::: "memory");
	s_add_i32 s73, 0, 0x18000
	s_add_i32 s74, 0, 0x1c000
	v_add_u32_e32 v14, s73, v188
	v_add_u32_e32 v30, s74, v188
	ds_read_b128 v[2:5], v14
	ds_read_b128 v[6:9], v14 offset:1024
	ds_read_b128 v[10:13], v14 offset:2048
	ds_read_b128 v[14:17], v14 offset:3072
	ds_read_b128 v[18:21], v30
	ds_read_b128 v[22:25], v30 offset:1024
	ds_read_b128 v[26:29], v30 offset:2048
	ds_read_b128 v[30:33], v30 offset:3072
	s_add_u32 s34, s34, 0xb0000
	s_addc_u32 s35, s35, 0
	s_mov_b32 m0, s41
	v_lshl_add_u64 v[186:187], s[34:35], 0, v[162:163]
	ds_read_b128 v[194:197], v192 offset:32768
	ds_read_b128 v[198:201], v192 offset:33792
	ds_read_b128 v[202:205], v192 offset:34816
	ds_read_b128 v[206:209], v192 offset:35840
	ds_read_b128 v[210:213], v192 offset:36864
	ds_read_b128 v[214:217], v192 offset:37888
	ds_read_b128 v[218:221], v192 offset:38912
	ds_read_b128 v[222:225], v192 offset:39936
	global_load_lds_dwordx4 v[186:187], off
	v_lshl_add_u64 v[186:187], s[34:35], 0, v[166:167]
	s_mov_b32 m0, s42
	s_nop 0
	global_load_lds_dwordx4 v[186:187], off
	s_waitcnt vmcnt(8)
	s_waitcnt lgkmcnt(0)
	s_barrier
	s_setprio 1
	s_waitcnt lgkmcnt(0)
	v_mfma_f32_16x16x128_f8f6f4 v[158:161], v[2:9], v[194:201], v[158:161]
	v_mfma_f32_16x16x128_f8f6f4 v[154:157], v[10:17], v[194:201], v[154:157]
	v_mfma_f32_16x16x128_f8f6f4 v[142:145], v[2:9], v[202:209], v[142:145]
	v_mfma_f32_16x16x128_f8f6f4 v[138:141], v[10:17], v[202:209], v[138:141]
	v_mfma_f32_16x16x128_f8f6f4 v[126:129], v[2:9], v[210:217], v[126:129]
	v_mfma_f32_16x16x128_f8f6f4 v[122:125], v[10:17], v[210:217], v[122:125]
	v_mfma_f32_16x16x128_f8f6f4 v[110:113], v[2:9], v[218:225], v[110:113]
	v_mfma_f32_16x16x128_f8f6f4 v[106:109], v[10:17], v[218:225], v[106:109]
	s_setprio 0
	s_setprio 1
	v_mfma_f32_16x16x128_f8f6f4 v[150:153], v[18:25], v[194:201], v[150:153]
	v_mfma_f32_16x16x128_f8f6f4 v[146:149], v[26:33], v[194:201], v[146:149]
	v_mfma_f32_16x16x128_f8f6f4 v[134:137], v[18:25], v[202:209], v[134:137]
	v_mfma_f32_16x16x128_f8f6f4 v[130:133], v[26:33], v[202:209], v[130:133]
	v_mfma_f32_16x16x128_f8f6f4 v[118:121], v[18:25], v[210:217], v[118:121]
	v_mfma_f32_16x16x128_f8f6f4 v[114:117], v[26:33], v[210:217], v[114:117]
	v_mfma_f32_16x16x128_f8f6f4 v[102:105], v[18:25], v[218:225], v[102:105]
	v_mfma_f32_16x16x128_f8f6f4 v[98:101], v[26:33], v[218:225], v[98:101]
	s_setprio 0
	s_barrier
	s_add_i32 s34, s73, s38
	v_lshl_add_u64 v[178:179], v[178:179], 0, s[12:13]
	s_mov_b32 m0, s34
	ds_read_b128 v[194:197], v192 offset:49152
	ds_read_b128 v[198:201], v192 offset:50176
	ds_read_b128 v[202:205], v192 offset:51200
	ds_read_b128 v[206:209], v192 offset:52224
	ds_read_b128 v[210:213], v192 offset:53248
	ds_read_b128 v[214:217], v192 offset:54272
	ds_read_b128 v[218:221], v192 offset:55296
	ds_read_b128 v[222:225], v192 offset:56320
	global_load_lds_dwordx4 v[178:179], off
	s_add_i32 m0, s34, 0x2000
	s_add_u32 s30, s30, 0xb0080
	v_lshl_add_u64 v[178:179], v[180:181], 0, s[12:13]
	s_addc_u32 s31, s31, 0
	s_add_i32 s34, s74, s38
	global_load_lds_dwordx4 v[178:179], off
	v_lshl_add_u64 v[178:179], s[30:31], 0, v[164:165]
	s_mov_b32 m0, s34
	s_nop 0
	global_load_lds_dwordx4 v[178:179], off
	v_lshl_add_u64 v[178:179], s[30:31], 0, v[168:169]
	s_add_i32 m0, s34, 0x2000
	s_nop 0
	global_load_lds_dwordx4 v[178:179], off
	v_lshl_add_u64 v[178:179], v[182:183], 0, s[12:13]
	s_mov_b32 m0, s47
	s_nop 0
	global_load_lds_dwordx4 v[178:179], off
	v_lshl_add_u64 v[178:179], v[184:185], 0, s[12:13]
	s_mov_b32 m0, s48
	s_nop 0
	global_load_lds_dwordx4 v[178:179], off
	s_waitcnt vmcnt(8)
	s_waitcnt lgkmcnt(0)
	s_barrier
	s_setprio 1
	s_waitcnt lgkmcnt(0)
	v_mfma_f32_16x16x128_f8f6f4 v[94:97], v[2:9], v[194:201], v[94:97]
	v_mfma_f32_16x16x128_f8f6f4 v[90:93], v[10:17], v[194:201], v[90:93]
	v_mfma_f32_16x16x128_f8f6f4 v[78:81], v[2:9], v[202:209], v[78:81]
	v_mfma_f32_16x16x128_f8f6f4 v[74:77], v[10:17], v[202:209], v[74:77]
	v_mfma_f32_16x16x128_f8f6f4 v[62:65], v[2:9], v[210:217], v[62:65]
	v_mfma_f32_16x16x128_f8f6f4 v[58:61], v[10:17], v[210:217], v[58:61]
	v_mfma_f32_16x16x128_f8f6f4 v[46:49], v[2:9], v[218:225], v[46:49]
	v_mfma_f32_16x16x128_f8f6f4 v[42:45], v[10:17], v[218:225], v[42:45]
	s_setprio 0
	s_setprio 1
	v_mfma_f32_16x16x128_f8f6f4 v[86:89], v[18:25], v[194:201], v[86:89]
	v_mfma_f32_16x16x128_f8f6f4 v[82:85], v[26:33], v[194:201], v[82:85]
	v_mfma_f32_16x16x128_f8f6f4 v[70:73], v[18:25], v[202:209], v[70:73]
	v_mfma_f32_16x16x128_f8f6f4 v[66:69], v[26:33], v[202:209], v[66:69]
	v_mfma_f32_16x16x128_f8f6f4 v[54:57], v[18:25], v[210:217], v[54:57]
	v_mfma_f32_16x16x128_f8f6f4 v[50:53], v[26:33], v[210:217], v[50:53]
	v_mfma_f32_16x16x128_f8f6f4 v[38:41], v[18:25], v[218:225], v[38:41]
	v_mfma_f32_16x16x128_f8f6f4 v[34:37], v[26:33], v[218:225], v[34:37]
	s_setprio 0
	s_add_i32 s72, s72, 2
	s_add_u32 s28, s28, 0x100
	s_addc_u32 s29, s29, 0
	s_add_u32 s70, s70, 0x100
	s_addc_u32 s71, s71, 0
	s_cmp_gt_u32 s72, 41
	s_barrier
	s_cbranch_scc0 .LBB0_1225
	s_nop 15
	s_nop 15
	s_nop 15
	s_nop 15
	s_and_b64 vcc, exec, s[14:15]
	s_cbranch_vccz .LBB0_1228
	s_barrier

; #define PG8_STAGE(bufoff, gbase, voff) do { _Pragma("unroll") for (int _i = 0; _i < 2; ++_i) \
;         __builtin_amdgcn_global_load_lds((const unsigned*)((const char*)(gbase) + (voff)[_i]), (PG8_LAS unsigned*)(lds + (bufoff) + ldsw + _i * 8192), 16, 0, 0); } while (0)
; #define PG8_LDA(dst, b, h) do { _Pragma("unroll") for (int m = 0; m < 4; ++m) _Pragma("unroll") for (int k = 0; k < 2; ++k) dst[m][k] = *(const PG8_LAS bf16x8*)(lds + PG8_SA(b, h) + aoff + m * 2048 + k * 1024); } while (0)
; #define PG8_LDB(dst, b, h) do { _Pragma("unroll") for (int n = 0; n < 2; ++n) _Pragma("unroll") for (int k = 0; k < 2; ++k) dst[n][k] = *(const PG8_LAS bf16x8*)(lds + PG8_SB(b, h) + boff + n * 2048 + k * 1024); } while (0)
; #define PG8_WAIT_V(n) asm volatile("s_waitcnt vmcnt(" #n ")" ::: "memory")
; #define PG8_WAIT_L(n) asm volatile("s_waitcnt lgkmcnt(" #n ")" ::: "memory")
; #define PG8_BAR __builtin_amdgcn_s_barrier()
; #define PG8_SCHED __builtin_amdgcn_sched_barrier(0)
; template <class Epi, class Sched, bool ALIGN_EPI = false, bool SP2 = false, bool FP8 = false>
; __device__ __forceinline__ void gemm_phase(PG8_LAS unsigned char* lds, const Gemm g, const Sched& S, const Epi& E) {
;     ...
;             PG8_LDB(B0, 0, 0); PG8_LDB(B1, 0, 1); PG8_SCHED; PG8_LDA(At, 0, 0); PG8_STAGE(PG8_SA(1, 1), a1 + hstep, voffA);
;             PG8_WAIT_V(8); PG8_WAIT_L(0); PG8_BAR; PG8_MMA(0, 0, At, B0); PG8_MMA(0, 1, At, B1); PG8_BAR; PG8_SCHED;
;             PG8_LDA(At, 0, 1); PG8_STAGE(PG8_SB(0, 0), b2, voffB); PG8_STAGE(PG8_SB(0, 1), b2 + hstep, voffB); PG8_STAGE(PG8_SA(0, 0), a2, voffA);
;             PG8_WAIT_V(8); PG8_WAIT_L(0); PG8_BAR; PG8_MMA(1, 0, At, B0); PG8_MMA(1, 1, At, B1); PG8_BAR; PG8_SCHED;
.LBB0_1358:
	ds_read_b128 v[146:149], v152
	ds_read_b128 v[156:159], v152 offset:1024
	ds_read_b128 v[160:163], v152 offset:2048
	ds_read_b128 v[164:167], v152 offset:3072
	ds_read_b128 v[168:171], v153
	ds_read_b128 v[172:175], v153 offset:1024
	ds_read_b128 v[176:179], v153 offset:2048
	ds_read_b128 v[180:183], v153 offset:3072
	s_add_u32 s26, s24, 0xfff80080
	s_addc_u32 s27, s25, -1
	s_cmp_eq_u32 s62, 28
	s_cselect_b32 s29, s17, s27
	s_cselect_b32 s28, s56, s26
	s_cselect_b32 s27, s15, s61
	s_cselect_b32 s26, s57, s60
	v_lshl_add_u64 v[216:217], s[24:25], 0, v[138:139]
	s_add_i32 m0, s23, 0xc000
	ds_read_b128 v[184:187], v154
	ds_read_b128 v[188:191], v154 offset:1024
	ds_read_b128 v[192:195], v154 offset:2048
	ds_read_b128 v[196:199], v154 offset:3072
	ds_read_b128 v[200:203], v154 offset:4096
	ds_read_b128 v[204:207], v154 offset:5120
	ds_read_b128 v[208:211], v154 offset:6144
	ds_read_b128 v[212:215], v154 offset:7168
	global_load_lds_dwordx4 v[216:217], off
	v_lshl_add_u64 v[216:217], s[24:25], 0, v[140:141]
	s_add_i32 m0, s23, 0xe000
	s_nop 0
	global_load_lds_dwordx4 v[216:217], off
	s_waitcnt vmcnt(8)
	s_waitcnt lgkmcnt(0)
	s_barrier
	s_setprio 1
	s_waitcnt lgkmcnt(0)
	v_mfma_f32_16x16x32_bf16 v[126:129], v[146:149], v[184:187], v[126:129]
	v_mfma_f32_16x16x32_bf16 v[122:125], v[160:163], v[184:187], v[122:125]
	v_mfma_f32_16x16x32_bf16 v[118:121], v[146:149], v[192:195], v[118:121]
	v_mfma_f32_16x16x32_bf16 v[110:113], v[160:163], v[192:195], v[110:113]
	v_mfma_f32_16x16x32_bf16 v[102:105], v[146:149], v[200:203], v[102:105]
	v_mfma_f32_16x16x32_bf16 v[94:97], v[160:163], v[200:203], v[94:97]
	v_mfma_f32_16x16x32_bf16 v[86:89], v[146:149], v[208:211], v[86:89]
	v_mfma_f32_16x16x32_bf16 v[78:81], v[160:163], v[208:211], v[78:81]
	v_mfma_f32_16x16x32_bf16 v[126:129], v[156:159], v[188:191], v[126:129]
	v_mfma_f32_16x16x32_bf16 v[122:125], v[164:167], v[188:191], v[122:125]
	v_mfma_f32_16x16x32_bf16 v[118:121], v[156:159], v[196:199], v[118:121]
	v_mfma_f32_16x16x32_bf16 v[110:113], v[164:167], v[196:199], v[110:113]
	v_mfma_f32_16x16x32_bf16 v[102:105], v[156:159], v[204:207], v[102:105]
	v_mfma_f32_16x16x32_bf16 v[94:97], v[164:167], v[204:207], v[94:97]
	v_mfma_f32_16x16x32_bf16 v[86:89], v[156:159], v[212:215], v[86:89]
	v_mfma_f32_16x16x32_bf16 v[78:81], v[164:167], v[212:215], v[78:81]
	s_setprio 0
	s_setprio 1
	v_mfma_f32_16x16x32_bf16 v[114:117], v[168:171], v[184:187], v[114:117]
	v_mfma_f32_16x16x32_bf16 v[106:109], v[176:179], v[184:187], v[106:109]
	v_mfma_f32_16x16x32_bf16 v[98:101], v[168:171], v[192:195], v[98:101]
	v_mfma_f32_16x16x32_bf16 v[90:93], v[176:179], v[192:195], v[90:93]
	v_mfma_f32_16x16x32_bf16 v[82:85], v[168:171], v[200:203], v[82:85]
	v_mfma_f32_16x16x32_bf16 v[74:77], v[176:179], v[200:203], v[74:77]
	v_mfma_f32_16x16x32_bf16 v[70:73], v[168:171], v[208:211], v[70:73]
	v_mfma_f32_16x16x32_bf16 v[66:69], v[176:179], v[208:211], v[66:69]
	v_mfma_f32_16x16x32_bf16 v[114:117], v[172:175], v[188:191], v[114:117]
	v_mfma_f32_16x16x32_bf16 v[106:109], v[180:183], v[188:191], v[106:109]
	v_mfma_f32_16x16x32_bf16 v[98:101], v[172:175], v[196:199], v[98:101]
	v_mfma_f32_16x16x32_bf16 v[90:93], v[180:183], v[196:199], v[90:93]
	v_mfma_f32_16x16x32_bf16 v[82:85], v[172:175], v[204:207], v[82:85]
	v_mfma_f32_16x16x32_bf16 v[74:77], v[180:183], v[204:207], v[74:77]
	v_mfma_f32_16x16x32_bf16 v[70:73], v[172:175], v[212:215], v[70:73]
	v_mfma_f32_16x16x32_bf16 v[66:69], v[180:183], v[212:215], v[66:69]
	s_setprio 0
	s_barrier
	s_add_i32 s63, s46, s35
	v_lshl_add_u64 v[216:217], s[26:27], 0, v[134:135]
	s_mov_b32 m0, s63
	ds_read_b128 v[184:187], v154 offset:16384
	ds_read_b128 v[188:191], v154 offset:17408
	ds_read_b128 v[192:195], v154 offset:18432
	ds_read_b128 v[196:199], v154 offset:19456
	ds_read_b128 v[200:203], v154 offset:20480
	ds_read_b128 v[204:207], v154 offset:21504
	ds_read_b128 v[208:211], v154 offset:22528
	ds_read_b128 v[212:215], v154 offset:23552
	global_load_lds_dwordx4 v[216:217], off
	s_add_i32 m0, s63, 0x2000
	s_add_u32 s68, s26, 0x80000
	v_lshl_add_u64 v[218:219], s[26:27], 0, v[130:131]
	s_addc_u32 s69, s27, 0
	s_add_i32 s63, s47, s35
	global_load_lds_dwordx4 v[218:219], off
	v_lshl_add_u64 v[220:221], s[68:69], 0, v[134:135]
	s_mov_b32 m0, s63
	v_lshl_add_u64 v[222:223], s[28:29], 0, v[132:133]
	global_load_lds_dwordx4 v[220:221], off
	v_lshl_add_u64 v[220:221], s[68:69], 0, v[130:131]
	s_add_i32 m0, s63, 0x2000
	s_nop 0
	global_load_lds_dwordx4 v[220:221], off
	v_lshl_add_u64 v[220:221], s[28:29], 0, v[136:137]
	s_mov_b32 m0, s23
	s_nop 0
	global_load_lds_dwordx4 v[220:221], off
	s_mov_b32 m0, s38
	s_nop 0
	global_load_lds_dwordx4 v[222:223], off
	s_waitcnt vmcnt(8)
	s_waitcnt lgkmcnt(0)
	s_barrier
; #define PG8_STAGE(bufoff, gbase, voff) do { _Pragma("unroll") for (int _i = 0; _i < 2; ++_i) \
;         __builtin_amdgcn_global_load_lds((const unsigned*)((const char*)(gbase) + (voff)[_i]), (PG8_LAS unsigned*)(lds + (bufoff) + ldsw + _i * 8192), 16, 0, 0); } while (0)
; #define PG8_LDA(dst, b, h) do { _Pragma("unroll") for (int m = 0; m < 4; ++m) _Pragma("unroll") for (int k = 0; k < 2; ++k) dst[m][k] = *(const PG8_LAS bf16x8*)(lds + PG8_SA(b, h) + aoff + m * 2048 + k * 1024); } while (0)
; #define PG8_LDB(dst, b, h) do { _Pragma("unroll") for (int n = 0; n < 2; ++n) _Pragma("unroll") for (int k = 0; k < 2; ++k) dst[n][k] = *(const PG8_LAS bf16x8*)(lds + PG8_SB(b, h) + boff + n * 2048 + k * 1024); } while (0)
; #define PG8_WAIT_V(n) asm volatile("s_waitcnt vmcnt(" #n ")" ::: "memory")
; #define PG8_WAIT_L(n) asm volatile("s_waitcnt lgkmcnt(" #n ")" ::: "memory")
; #define PG8_BAR __builtin_amdgcn_s_barrier()
; #define PG8_SCHED __builtin_amdgcn_sched_barrier(0)
; template <class Epi, class Sched, bool ALIGN_EPI = false, bool SP2 = false, bool FP8 = false>
; __device__ __forceinline__ void gemm_phase(PG8_LAS unsigned char* lds, const Gemm g, const Sched& S, const Epi& E) {
;     ...
;             PG8_WAIT_V(8); PG8_WAIT_L(0); PG8_BAR; PG8_MMA(1, 0, At, B0); PG8_MMA(1, 1, At, B1); PG8_BAR; PG8_SCHED;
;             PG8_LDB(B0, 1, 0); PG8_LDB(B1, 1, 1); PG8_SCHED; PG8_LDA(At, 1, 0); PG8_STAGE(PG8_SA(0, 1), a2 + hstep, voffA);
;             PG8_WAIT_V(8); PG8_WAIT_L(0); PG8_BAR; PG8_MMA(0, 0, At, B0); PG8_MMA(0, 1, At, B1); PG8_BAR; PG8_SCHED;
	s_setprio 1
	s_waitcnt lgkmcnt(0)
	v_mfma_f32_16x16x32_bf16 v[62:65], v[146:149], v[184:187], v[62:65]
	v_mfma_f32_16x16x32_bf16 v[58:61], v[160:163], v[184:187], v[58:61]
	v_mfma_f32_16x16x32_bf16 v[54:57], v[146:149], v[192:195], v[54:57]
	v_mfma_f32_16x16x32_bf16 v[46:49], v[160:163], v[192:195], v[46:49]
	v_mfma_f32_16x16x32_bf16 v[38:41], v[146:149], v[200:203], v[38:41]
	v_mfma_f32_16x16x32_bf16 v[30:33], v[160:163], v[200:203], v[30:33]
	v_mfma_f32_16x16x32_bf16 v[22:25], v[146:149], v[208:211], v[22:25]
	v_mfma_f32_16x16x32_bf16 v[14:17], v[160:163], v[208:211], v[14:17]
	v_mfma_f32_16x16x32_bf16 v[62:65], v[156:159], v[188:191], v[62:65]
	v_mfma_f32_16x16x32_bf16 v[58:61], v[164:167], v[188:191], v[58:61]
	v_mfma_f32_16x16x32_bf16 v[54:57], v[156:159], v[196:199], v[54:57]
	v_mfma_f32_16x16x32_bf16 v[46:49], v[164:167], v[196:199], v[46:49]
	v_mfma_f32_16x16x32_bf16 v[38:41], v[156:159], v[204:207], v[38:41]
	v_mfma_f32_16x16x32_bf16 v[30:33], v[164:167], v[204:207], v[30:33]
	v_mfma_f32_16x16x32_bf16 v[22:25], v[156:159], v[212:215], v[22:25]
	v_mfma_f32_16x16x32_bf16 v[14:17], v[164:167], v[212:215], v[14:17]
	s_setprio 0
	s_setprio 1
	v_mfma_f32_16x16x32_bf16 v[50:53], v[168:171], v[184:187], v[50:53]
	v_mfma_f32_16x16x32_bf16 v[42:45], v[176:179], v[184:187], v[42:45]
	v_mfma_f32_16x16x32_bf16 v[34:37], v[168:171], v[192:195], v[34:37]
	v_mfma_f32_16x16x32_bf16 v[26:29], v[176:179], v[192:195], v[26:29]
	v_mfma_f32_16x16x32_bf16 v[18:21], v[168:171], v[200:203], v[18:21]
	v_mfma_f32_16x16x32_bf16 v[10:13], v[176:179], v[200:203], v[10:13]
	v_mfma_f32_16x16x32_bf16 v[6:9], v[168:171], v[208:211], v[6:9]
	v_mfma_f32_16x16x32_bf16 v[2:5], v[176:179], v[208:211], v[2:5]
	v_mfma_f32_16x16x32_bf16 v[50:53], v[172:175], v[188:191], v[50:53]
	v_mfma_f32_16x16x32_bf16 v[42:45], v[180:183], v[188:191], v[42:45]
	v_mfma_f32_16x16x32_bf16 v[34:37], v[172:175], v[196:199], v[34:37]
	v_mfma_f32_16x16x32_bf16 v[26:29], v[180:183], v[196:199], v[26:29]
	v_mfma_f32_16x16x32_bf16 v[18:21], v[172:175], v[204:207], v[18:21]
	v_mfma_f32_16x16x32_bf16 v[10:13], v[180:183], v[204:207], v[10:13]
	v_mfma_f32_16x16x32_bf16 v[6:9], v[172:175], v[212:215], v[6:9]
	v_mfma_f32_16x16x32_bf16 v[2:5], v[180:183], v[212:215], v[2:5]
	s_setprio 0
	s_barrier
	s_add_i32 s63, 0, 0x18000
	v_add_u32_e32 v155, s63, v150
	s_add_i32 s68, 0, 0x1c000
	ds_read_b128 v[146:149], v155
	ds_read_b128 v[156:159], v155 offset:1024
	ds_read_b128 v[160:163], v155 offset:2048
	ds_read_b128 v[164:167], v155 offset:3072
	v_add_u32_e32 v155, s68, v150
	ds_read_b128 v[168:171], v155
	ds_read_b128 v[172:175], v155 offset:1024
	ds_read_b128 v[176:179], v155 offset:2048
	ds_read_b128 v[180:183], v155 offset:3072
	s_add_u32 s28, s28, 0x80000
	s_addc_u32 s29, s29, 0
	s_mov_b32 m0, s39
	v_lshl_add_u64 v[224:225], s[28:29], 0, v[136:137]
	ds_read_b128 v[184:187], v154 offset:32768
	ds_read_b128 v[188:191], v154 offset:33792
	ds_read_b128 v[192:195], v154 offset:34816
	ds_read_b128 v[196:199], v154 offset:35840
	ds_read_b128 v[200:203], v154 offset:36864
	ds_read_b128 v[204:207], v154 offset:37888
	ds_read_b128 v[208:211], v154 offset:38912
	ds_read_b128 v[212:215], v154 offset:39936
	global_load_lds_dwordx4 v[224:225], off
	v_lshl_add_u64 v[224:225], s[28:29], 0, v[132:133]
	s_mov_b32 m0, s40
	s_nop 0
	global_load_lds_dwordx4 v[224:225], off
	s_waitcnt vmcnt(8)
	s_waitcnt lgkmcnt(0)
	s_barrier
	s_setprio 1
	s_waitcnt lgkmcnt(0)
	v_mfma_f32_16x16x32_bf16 v[126:129], v[146:149], v[184:187], v[126:129]
	v_mfma_f32_16x16x32_bf16 v[122:125], v[160:163], v[184:187], v[122:125]
	v_mfma_f32_16x16x32_bf16 v[118:121], v[146:149], v[192:195], v[118:121]
	v_mfma_f32_16x16x32_bf16 v[110:113], v[160:163], v[192:195], v[110:113]
	v_mfma_f32_16x16x32_bf16 v[102:105], v[146:149], v[200:203], v[102:105]
	v_mfma_f32_16x16x32_bf16 v[94:97], v[160:163], v[200:203], v[94:97]
	v_mfma_f32_16x16x32_bf16 v[86:89], v[146:149], v[208:211], v[86:89]
	v_mfma_f32_16x16x32_bf16 v[78:81], v[160:163], v[208:211], v[78:81]
	v_mfma_f32_16x16x32_bf16 v[126:129], v[156:159], v[188:191], v[126:129]
	v_mfma_f32_16x16x32_bf16 v[122:125], v[164:167], v[188:191], v[122:125]
	v_mfma_f32_16x16x32_bf16 v[118:121], v[156:159], v[196:199], v[118:121]
	v_mfma_f32_16x16x32_bf16 v[110:113], v[164:167], v[196:199], v[110:113]
	v_mfma_f32_16x16x32_bf16 v[102:105], v[156:159], v[204:207], v[102:105]
	v_mfma_f32_16x16x32_bf16 v[94:97], v[164:167], v[204:207], v[94:97]
	v_mfma_f32_16x16x32_bf16 v[86:89], v[156:159], v[212:215], v[86:89]
	v_mfma_f32_16x16x32_bf16 v[78:81], v[164:167], v[212:215], v[78:81]
	s_setprio 0
	s_setprio 1
	v_mfma_f32_16x16x32_bf16 v[114:117], v[168:171], v[184:187], v[114:117]
	v_mfma_f32_16x16x32_bf16 v[106:109], v[176:179], v[184:187], v[106:109]
	v_mfma_f32_16x16x32_bf16 v[98:101], v[168:171], v[192:195], v[98:101]
	v_mfma_f32_16x16x32_bf16 v[90:93], v[176:179], v[192:195], v[90:93]
	v_mfma_f32_16x16x32_bf16 v[82:85], v[168:171], v[200:203], v[82:85]
	v_mfma_f32_16x16x32_bf16 v[74:77], v[176:179], v[200:203], v[74:77]
	v_mfma_f32_16x16x32_bf16 v[70:73], v[168:171], v[208:211], v[70:73]
	v_mfma_f32_16x16x32_bf16 v[66:69], v[176:179], v[208:211], v[66:69]
	v_mfma_f32_16x16x32_bf16 v[114:117], v[172:175], v[188:191], v[114:117]
	v_mfma_f32_16x16x32_bf16 v[106:109], v[180:183], v[188:191], v[106:109]
	v_mfma_f32_16x16x32_bf16 v[98:101], v[172:175], v[196:199], v[98:101]
	v_mfma_f32_16x16x32_bf16 v[90:93], v[180:183], v[196:199], v[90:93]
	v_mfma_f32_16x16x32_bf16 v[82:85], v[172:175], v[204:207], v[82:85]
	v_mfma_f32_16x16x32_bf16 v[74:77], v[180:183], v[204:207], v[74:77]
	v_mfma_f32_16x16x32_bf16 v[70:73], v[172:175], v[212:215], v[70:73]
	v_mfma_f32_16x16x32_bf16 v[66:69], v[180:183], v[212:215], v[66:69]
	s_setprio 0
	s_barrier
; #define PG8_STAGE(bufoff, gbase, voff) do { _Pragma("unroll") for (int _i = 0; _i < 2; ++_i) \
;         __builtin_amdgcn_global_load_lds((const unsigned*)((const char*)(gbase) + (voff)[_i]), (PG8_LAS unsigned*)(lds + (bufoff) + ldsw + _i * 8192), 16, 0, 0); } while (0)
; #define PG8_LDA(dst, b, h) do { _Pragma("unroll") for (int m = 0; m < 4; ++m) _Pragma("unroll") for (int k = 0; k < 2; ++k) dst[m][k] = *(const PG8_LAS bf16x8*)(lds + PG8_SA(b, h) + aoff + m * 2048 + k * 1024); } while (0)
; #define PG8_WAIT_V(n) asm volatile("s_waitcnt vmcnt(" #n ")" ::: "memory")
; #define PG8_WAIT_L(n) asm volatile("s_waitcnt lgkmcnt(" #n ")" ::: "memory")
; #define PG8_BAR __builtin_amdgcn_s_barrier()
; #define PG8_SCHED __builtin_amdgcn_sched_barrier(0)
; template <class Epi, class Sched, bool ALIGN_EPI = false, bool SP2 = false, bool FP8 = false>
; __device__ __forceinline__ void gemm_phase(PG8_LAS unsigned char* lds, const Gemm g, const Sched& S, const Epi& E) {
;     ...
;         for (int t = 0; t < nt; t += 2) {
;             const bool last = (t == nt - 2);
;             const char* a1 = cA + (size_t)(t + 1) * kstep;
;             const char* a2 = last ? nA : cA + (size_t)(t + 2) * kstep; const char* b2 = last ? nB : cB + (size_t)(t + 2) * kstep;
;     ...
;             PG8_LDA(At, 1, 1); PG8_STAGE(PG8_SB(1, 0), b3, voffB); PG8_STAGE(PG8_SB(1, 1), b3 + hstep, voffB); PG8_STAGE(PG8_SA(1, 0), a3, voffA);
;             PG8_WAIT_V(8); PG8_WAIT_L(0); PG8_BAR; PG8_MMA(1, 0, At, B0); PG8_MMA(1, 1, At, B1); PG8_BAR; PG8_SCHED;
	s_add_i32 s28, s63, s35
	v_lshl_add_u64 v[216:217], v[216:217], 0, s[10:11]
	s_mov_b32 m0, s28
	ds_read_b128 v[184:187], v154 offset:49152
	ds_read_b128 v[188:191], v154 offset:50176
	ds_read_b128 v[192:195], v154 offset:51200
	ds_read_b128 v[196:199], v154 offset:52224
	ds_read_b128 v[200:203], v154 offset:53248
	ds_read_b128 v[204:207], v154 offset:54272
	ds_read_b128 v[208:211], v154 offset:55296
	ds_read_b128 v[212:215], v154 offset:56320
	global_load_lds_dwordx4 v[216:217], off
	s_add_i32 m0, s28, 0x2000
	s_add_u32 s26, s26, 0x80080
	v_lshl_add_u64 v[216:217], v[218:219], 0, s[10:11]
	s_addc_u32 s27, s27, 0
	s_add_i32 s28, s68, s35
	global_load_lds_dwordx4 v[216:217], off
	v_lshl_add_u64 v[216:217], s[26:27], 0, v[134:135]
	s_mov_b32 m0, s28
	s_nop 0
	global_load_lds_dwordx4 v[216:217], off
	v_lshl_add_u64 v[216:217], s[26:27], 0, v[130:131]
	s_add_i32 m0, s28, 0x2000
	s_nop 0
	global_load_lds_dwordx4 v[216:217], off
	v_lshl_add_u64 v[216:217], v[220:221], 0, s[10:11]
	s_mov_b32 m0, s43
	s_nop 0
	global_load_lds_dwordx4 v[216:217], off
	v_lshl_add_u64 v[216:217], v[222:223], 0, s[10:11]
	s_mov_b32 m0, s44
	s_nop 0
	global_load_lds_dwordx4 v[216:217], off
	s_waitcnt vmcnt(8)
	s_waitcnt lgkmcnt(0)
	s_barrier
	s_setprio 1
	s_waitcnt lgkmcnt(0)
	v_mfma_f32_16x16x32_bf16 v[62:65], v[146:149], v[184:187], v[62:65]
	v_mfma_f32_16x16x32_bf16 v[58:61], v[160:163], v[184:187], v[58:61]
	v_mfma_f32_16x16x32_bf16 v[54:57], v[146:149], v[192:195], v[54:57]
	v_mfma_f32_16x16x32_bf16 v[46:49], v[160:163], v[192:195], v[46:49]
	v_mfma_f32_16x16x32_bf16 v[38:41], v[146:149], v[200:203], v[38:41]
	v_mfma_f32_16x16x32_bf16 v[30:33], v[160:163], v[200:203], v[30:33]
	v_mfma_f32_16x16x32_bf16 v[22:25], v[146:149], v[208:211], v[22:25]
	v_mfma_f32_16x16x32_bf16 v[14:17], v[160:163], v[208:211], v[14:17]
	v_mfma_f32_16x16x32_bf16 v[62:65], v[156:159], v[188:191], v[62:65]
	v_mfma_f32_16x16x32_bf16 v[58:61], v[164:167], v[188:191], v[58:61]
	v_mfma_f32_16x16x32_bf16 v[54:57], v[156:159], v[196:199], v[54:57]
	v_mfma_f32_16x16x32_bf16 v[46:49], v[164:167], v[196:199], v[46:49]
	v_mfma_f32_16x16x32_bf16 v[38:41], v[156:159], v[204:207], v[38:41]
	v_mfma_f32_16x16x32_bf16 v[30:33], v[164:167], v[204:207], v[30:33]
	v_mfma_f32_16x16x32_bf16 v[22:25], v[156:159], v[212:215], v[22:25]
	v_mfma_f32_16x16x32_bf16 v[14:17], v[164:167], v[212:215], v[14:17]
	s_setprio 0
	s_setprio 1
	v_mfma_f32_16x16x32_bf16 v[50:53], v[168:171], v[184:187], v[50:53]
	v_mfma_f32_16x16x32_bf16 v[42:45], v[176:179], v[184:187], v[42:45]
	v_mfma_f32_16x16x32_bf16 v[34:37], v[168:171], v[192:195], v[34:37]
	v_mfma_f32_16x16x32_bf16 v[26:29], v[176:179], v[192:195], v[26:29]
	v_mfma_f32_16x16x32_bf16 v[18:21], v[168:171], v[200:203], v[18:21]
	v_mfma_f32_16x16x32_bf16 v[10:13], v[176:179], v[200:203], v[10:13]
	v_mfma_f32_16x16x32_bf16 v[6:9], v[168:171], v[208:211], v[6:9]
	v_mfma_f32_16x16x32_bf16 v[2:5], v[176:179], v[208:211], v[2:5]
	v_mfma_f32_16x16x32_bf16 v[50:53], v[172:175], v[188:191], v[50:53]
	v_mfma_f32_16x16x32_bf16 v[42:45], v[180:183], v[188:191], v[42:45]
	v_mfma_f32_16x16x32_bf16 v[34:37], v[172:175], v[196:199], v[34:37]
	v_mfma_f32_16x16x32_bf16 v[26:29], v[180:183], v[196:199], v[26:29]
	v_mfma_f32_16x16x32_bf16 v[18:21], v[172:175], v[204:207], v[18:21]
	v_mfma_f32_16x16x32_bf16 v[10:13], v[180:183], v[204:207], v[10:13]
	v_mfma_f32_16x16x32_bf16 v[6:9], v[172:175], v[212:215], v[6:9]
	v_mfma_f32_16x16x32_bf16 v[2:5], v[180:183], v[212:215], v[2:5]
	s_setprio 0
	s_add_i32 s62, s62, 2
	s_add_u32 s24, s24, 0x100
	s_addc_u32 s25, s25, 0
	s_add_u32 s60, s60, 0x100
	s_addc_u32 s61, s61, 0
	s_cmp_gt_u32 s62, 29
	s_barrier
	s_cbranch_scc0 .LBB0_1358
	s_and_b64 vcc, exec, s[12:13]
	s_cbranch_vccz .LBB0_1361
	s_barrier

; #define PG8_STAGE(bufoff, gbase, voff) do { _Pragma("unroll") for (int _i = 0; _i < 2; ++_i) \
;         __builtin_amdgcn_global_load_lds((const unsigned*)((const char*)(gbase) + (voff)[_i]), (PG8_LAS unsigned*)(lds + (bufoff) + ldsw + _i * 8192), 16, 0, 0); } while (0)
; #define PG8_LDA(dst, b, h) do { _Pragma("unroll") for (int m = 0; m < 4; ++m) _Pragma("unroll") for (int k = 0; k < 2; ++k) dst[m][k] = *(const PG8_LAS bf16x8*)(lds + PG8_SA(b, h) + aoff + m * 2048 + k * 1024); } while (0)
; #define PG8_LDB(dst, b, h) do { _Pragma("unroll") for (int n = 0; n < 2; ++n) _Pragma("unroll") for (int k = 0; k < 2; ++k) dst[n][k] = *(const PG8_LAS bf16x8*)(lds + PG8_SB(b, h) + boff + n * 2048 + k * 1024); } while (0)
; #define PG8_WAIT_V(n) asm volatile("s_waitcnt vmcnt(" #n ")" ::: "memory")
; #define PG8_WAIT_L(n) asm volatile("s_waitcnt lgkmcnt(" #n ")" ::: "memory")
; #define PG8_BAR __builtin_amdgcn_s_barrier()
; #define PG8_SCHED __builtin_amdgcn_sched_barrier(0)
; template <class Epi, class Sched, bool ALIGN_EPI = false, bool SP2 = false, bool FP8 = false>
; __device__ __forceinline__ void gemm_phase(PG8_LAS unsigned char* lds, const Gemm g, const Sched& S, const Epi& E) {
;     ...
;             PG8_LDB(B0, 0, 0); PG8_LDB(B1, 0, 1); PG8_SCHED; PG8_LDA(At, 0, 0); PG8_STAGE(PG8_SA(1, 1), a1 + hstep, voffA);
;             PG8_WAIT_V(8); PG8_WAIT_L(0); PG8_BAR; PG8_MMA(0, 0, At, B0); PG8_MMA(0, 1, At, B1); PG8_BAR; PG8_SCHED;
;             PG8_LDA(At, 0, 1); PG8_STAGE(PG8_SB(0, 0), b2, voffB); PG8_STAGE(PG8_SB(0, 1), b2 + hstep, voffB); PG8_STAGE(PG8_SA(0, 0), a2, voffA);
;             PG8_WAIT_V(8); PG8_WAIT_L(0); PG8_BAR; PG8_MMA(1, 0, At, B0); PG8_MMA(1, 1, At, B1); PG8_BAR; PG8_SCHED;
.LBB0_1952:
	ds_read_b128 v[130:133], v190
	ds_read_b128 v[134:137], v190 offset:1024
	ds_read_b128 v[138:141], v190 offset:2048
	ds_read_b128 v[142:145], v190 offset:3072
	ds_read_b128 v[162:165], v191
	ds_read_b128 v[166:169], v191 offset:1024
	ds_read_b128 v[170:173], v191 offset:2048
	ds_read_b128 v[174:177], v191 offset:3072
	s_add_u32 s36, s34, 0xfff80080
	s_addc_u32 s37, s35, -1
	s_cmp_eq_u32 s69, 28
	s_cselect_b32 s39, s25, s37
	s_cselect_b32 s38, s61, s36
	s_cselect_b32 s37, s23, s68
	s_cselect_b32 s36, s62, s63
	v_lshl_add_u64 v[186:187], s[34:35], 0, v[154:155]
	s_add_i32 m0, s31, 0xc000
	ds_read_b128 v[178:181], v192
	ds_read_b128 v[182:185], v192 offset:1024
	ds_read_b128 v[194:197], v192 offset:2048
	ds_read_b128 v[198:201], v192 offset:3072
	ds_read_b128 v[202:205], v192 offset:4096
	ds_read_b128 v[206:209], v192 offset:5120
	ds_read_b128 v[210:213], v192 offset:6144
	ds_read_b128 v[214:217], v192 offset:7168
	global_load_lds_dwordx4 v[186:187], off
	v_lshl_add_u64 v[186:187], s[34:35], 0, v[156:157]
	s_add_i32 m0, s31, 0xe000
	s_nop 0
	global_load_lds_dwordx4 v[186:187], off
	s_waitcnt vmcnt(8)
	s_waitcnt lgkmcnt(0)
	s_barrier
	s_setprio 1
	s_waitcnt lgkmcnt(0)
	v_mfma_f32_16x16x32_bf16 v[126:129], v[130:133], v[178:181], v[126:129]
	v_mfma_f32_16x16x32_bf16 v[122:125], v[138:141], v[178:181], v[122:125]
	v_mfma_f32_16x16x32_bf16 v[110:113], v[130:133], v[194:197], v[110:113]
	v_mfma_f32_16x16x32_bf16 v[106:109], v[138:141], v[194:197], v[106:109]
	v_mfma_f32_16x16x32_bf16 v[94:97], v[130:133], v[202:205], v[94:97]
	v_mfma_f32_16x16x32_bf16 v[90:93], v[138:141], v[202:205], v[90:93]
	v_mfma_f32_16x16x32_bf16 v[78:81], v[130:133], v[210:213], v[78:81]
	v_mfma_f32_16x16x32_bf16 v[74:77], v[138:141], v[210:213], v[74:77]
	v_mfma_f32_16x16x32_bf16 v[126:129], v[134:137], v[182:185], v[126:129]
	v_mfma_f32_16x16x32_bf16 v[122:125], v[142:145], v[182:185], v[122:125]
	v_mfma_f32_16x16x32_bf16 v[110:113], v[134:137], v[198:201], v[110:113]
	v_mfma_f32_16x16x32_bf16 v[106:109], v[142:145], v[198:201], v[106:109]
	v_mfma_f32_16x16x32_bf16 v[94:97], v[134:137], v[206:209], v[94:97]
	v_mfma_f32_16x16x32_bf16 v[90:93], v[142:145], v[206:209], v[90:93]
	v_mfma_f32_16x16x32_bf16 v[78:81], v[134:137], v[214:217], v[78:81]
	v_mfma_f32_16x16x32_bf16 v[74:77], v[142:145], v[214:217], v[74:77]
	s_setprio 0
	s_setprio 1
	v_mfma_f32_16x16x32_bf16 v[118:121], v[162:165], v[178:181], v[118:121]
	v_mfma_f32_16x16x32_bf16 v[114:117], v[170:173], v[178:181], v[114:117]
	v_mfma_f32_16x16x32_bf16 v[102:105], v[162:165], v[194:197], v[102:105]
	v_mfma_f32_16x16x32_bf16 v[98:101], v[170:173], v[194:197], v[98:101]
	v_mfma_f32_16x16x32_bf16 v[86:89], v[162:165], v[202:205], v[86:89]
	v_mfma_f32_16x16x32_bf16 v[82:85], v[170:173], v[202:205], v[82:85]
	v_mfma_f32_16x16x32_bf16 v[70:73], v[162:165], v[210:213], v[70:73]
	v_mfma_f32_16x16x32_bf16 v[66:69], v[170:173], v[210:213], v[66:69]
	v_mfma_f32_16x16x32_bf16 v[118:121], v[166:169], v[182:185], v[118:121]
	v_mfma_f32_16x16x32_bf16 v[114:117], v[174:177], v[182:185], v[114:117]
	v_mfma_f32_16x16x32_bf16 v[102:105], v[166:169], v[198:201], v[102:105]
	v_mfma_f32_16x16x32_bf16 v[98:101], v[174:177], v[198:201], v[98:101]
	v_mfma_f32_16x16x32_bf16 v[86:89], v[166:169], v[206:209], v[86:89]
	v_mfma_f32_16x16x32_bf16 v[82:85], v[174:177], v[206:209], v[82:85]
	v_mfma_f32_16x16x32_bf16 v[70:73], v[166:169], v[214:217], v[70:73]
	v_mfma_f32_16x16x32_bf16 v[66:69], v[174:177], v[214:217], v[66:69]
	s_setprio 0
	s_barrier
	s_add_i32 s70, s54, s43
	v_lshl_add_u64 v[186:187], s[36:37], 0, v[148:149]
	s_mov_b32 m0, s70
	ds_read_b128 v[178:181], v192 offset:16384
	ds_read_b128 v[182:185], v192 offset:17408
	ds_read_b128 v[194:197], v192 offset:18432
	ds_read_b128 v[198:201], v192 offset:19456
	ds_read_b128 v[202:205], v192 offset:20480
	ds_read_b128 v[206:209], v192 offset:21504
	ds_read_b128 v[210:213], v192 offset:22528
	ds_read_b128 v[214:217], v192 offset:23552
	global_load_lds_dwordx4 v[186:187], off
	s_add_i32 m0, s70, 0x2000
	s_add_u32 s70, s36, 0x80000
	v_lshl_add_u64 v[218:219], s[36:37], 0, v[152:153]
	s_addc_u32 s71, s37, 0
	s_add_i32 s72, s55, s43
	global_load_lds_dwordx4 v[218:219], off
	v_lshl_add_u64 v[220:221], s[70:71], 0, v[148:149]
	s_mov_b32 m0, s72
	v_lshl_add_u64 v[222:223], s[38:39], 0, v[150:151]
	global_load_lds_dwordx4 v[220:221], off
	v_lshl_add_u64 v[220:221], s[70:71], 0, v[152:153]
	s_add_i32 m0, s72, 0x2000
	s_nop 0
	global_load_lds_dwordx4 v[220:221], off
	v_lshl_add_u64 v[220:221], s[38:39], 0, v[146:147]
	s_mov_b32 m0, s31
	s_nop 0
	global_load_lds_dwordx4 v[220:221], off
	s_mov_b32 m0, s44
	s_nop 0
	global_load_lds_dwordx4 v[222:223], off
	s_waitcnt vmcnt(8)
	s_waitcnt lgkmcnt(0)
	s_barrier
; #define PG8_STAGE(bufoff, gbase, voff) do { _Pragma("unroll") for (int _i = 0; _i < 2; ++_i) \
;         __builtin_amdgcn_global_load_lds((const unsigned*)((const char*)(gbase) + (voff)[_i]), (PG8_LAS unsigned*)(lds + (bufoff) + ldsw + _i * 8192), 16, 0, 0); } while (0)
; #define PG8_LDA(dst, b, h) do { _Pragma("unroll") for (int m = 0; m < 4; ++m) _Pragma("unroll") for (int k = 0; k < 2; ++k) dst[m][k] = *(const PG8_LAS bf16x8*)(lds + PG8_SA(b, h) + aoff + m * 2048 + k * 1024); } while (0)
; #define PG8_LDB(dst, b, h) do { _Pragma("unroll") for (int n = 0; n < 2; ++n) _Pragma("unroll") for (int k = 0; k < 2; ++k) dst[n][k] = *(const PG8_LAS bf16x8*)(lds + PG8_SB(b, h) + boff + n * 2048 + k * 1024); } while (0)
; #define PG8_WAIT_V(n) asm volatile("s_waitcnt vmcnt(" #n ")" ::: "memory")
; #define PG8_WAIT_L(n) asm volatile("s_waitcnt lgkmcnt(" #n ")" ::: "memory")
; #define PG8_BAR __builtin_amdgcn_s_barrier()
; #define PG8_SCHED __builtin_amdgcn_sched_barrier(0)
; template <class Epi, class Sched, bool ALIGN_EPI = false, bool SP2 = false, bool FP8 = false>
; __device__ __forceinline__ void gemm_phase(PG8_LAS unsigned char* lds, const Gemm g, const Sched& S, const Epi& E) {
;     ...
;             PG8_WAIT_V(8); PG8_WAIT_L(0); PG8_BAR; PG8_MMA(1, 0, At, B0); PG8_MMA(1, 1, At, B1); PG8_BAR; PG8_SCHED;
;             PG8_LDB(B0, 1, 0); PG8_LDB(B1, 1, 1); PG8_SCHED; PG8_LDA(At, 1, 0); PG8_STAGE(PG8_SA(0, 1), a2 + hstep, voffA);
;             PG8_WAIT_V(8); PG8_WAIT_L(0); PG8_BAR; PG8_MMA(0, 0, At, B0); PG8_MMA(0, 1, At, B1); PG8_BAR; PG8_SCHED;
	s_setprio 1
	s_waitcnt lgkmcnt(0)
	v_mfma_f32_16x16x32_bf16 v[62:65], v[130:133], v[178:181], v[62:65]
	v_mfma_f32_16x16x32_bf16 v[58:61], v[138:141], v[178:181], v[58:61]
	v_mfma_f32_16x16x32_bf16 v[46:49], v[130:133], v[194:197], v[46:49]
	v_mfma_f32_16x16x32_bf16 v[42:45], v[138:141], v[194:197], v[42:45]
	v_mfma_f32_16x16x32_bf16 v[30:33], v[130:133], v[202:205], v[30:33]
	v_mfma_f32_16x16x32_bf16 v[26:29], v[138:141], v[202:205], v[26:29]
	v_mfma_f32_16x16x32_bf16 v[14:17], v[130:133], v[210:213], v[14:17]
	v_mfma_f32_16x16x32_bf16 v[10:13], v[138:141], v[210:213], v[10:13]
	v_mfma_f32_16x16x32_bf16 v[62:65], v[134:137], v[182:185], v[62:65]
	v_mfma_f32_16x16x32_bf16 v[58:61], v[142:145], v[182:185], v[58:61]
	v_mfma_f32_16x16x32_bf16 v[46:49], v[134:137], v[198:201], v[46:49]
	v_mfma_f32_16x16x32_bf16 v[42:45], v[142:145], v[198:201], v[42:45]
	v_mfma_f32_16x16x32_bf16 v[30:33], v[134:137], v[206:209], v[30:33]
	v_mfma_f32_16x16x32_bf16 v[26:29], v[142:145], v[206:209], v[26:29]
	v_mfma_f32_16x16x32_bf16 v[14:17], v[134:137], v[214:217], v[14:17]
	v_mfma_f32_16x16x32_bf16 v[10:13], v[142:145], v[214:217], v[10:13]
	s_setprio 0
	s_setprio 1
	v_mfma_f32_16x16x32_bf16 v[54:57], v[162:165], v[178:181], v[54:57]
	v_mfma_f32_16x16x32_bf16 v[50:53], v[170:173], v[178:181], v[50:53]
	v_mfma_f32_16x16x32_bf16 v[38:41], v[162:165], v[194:197], v[38:41]
	v_mfma_f32_16x16x32_bf16 v[34:37], v[170:173], v[194:197], v[34:37]
	v_mfma_f32_16x16x32_bf16 v[22:25], v[162:165], v[202:205], v[22:25]
	v_mfma_f32_16x16x32_bf16 v[18:21], v[170:173], v[202:205], v[18:21]
	v_mfma_f32_16x16x32_bf16 v[6:9], v[162:165], v[210:213], v[6:9]
	v_mfma_f32_16x16x32_bf16 v[2:5], v[170:173], v[210:213], v[2:5]
	v_mfma_f32_16x16x32_bf16 v[54:57], v[166:169], v[182:185], v[54:57]
	v_mfma_f32_16x16x32_bf16 v[50:53], v[174:177], v[182:185], v[50:53]
	v_mfma_f32_16x16x32_bf16 v[38:41], v[166:169], v[198:201], v[38:41]
	v_mfma_f32_16x16x32_bf16 v[34:37], v[174:177], v[198:201], v[34:37]
	v_mfma_f32_16x16x32_bf16 v[22:25], v[166:169], v[206:209], v[22:25]
	v_mfma_f32_16x16x32_bf16 v[18:21], v[174:177], v[206:209], v[18:21]
	v_mfma_f32_16x16x32_bf16 v[6:9], v[166:169], v[214:217], v[6:9]
	v_mfma_f32_16x16x32_bf16 v[2:5], v[174:177], v[214:217], v[2:5]
	s_setprio 0
	s_barrier
	s_add_i32 s70, 0, 0x18000
	s_add_i32 s71, 0, 0x1c000
	v_add_u32_e32 v142, s70, v188
	v_add_u32_e32 v174, s71, v188
	ds_read_b128 v[130:133], v142
	ds_read_b128 v[134:137], v142 offset:1024
	ds_read_b128 v[138:141], v142 offset:2048
	ds_read_b128 v[142:145], v142 offset:3072
	ds_read_b128 v[162:165], v174
	ds_read_b128 v[166:169], v174 offset:1024
	ds_read_b128 v[170:173], v174 offset:2048
	ds_read_b128 v[174:177], v174 offset:3072
	s_add_u32 s38, s38, 0x80000
	s_addc_u32 s39, s39, 0
	s_mov_b32 m0, s45
	v_lshl_add_u64 v[224:225], s[38:39], 0, v[146:147]
	ds_read_b128 v[178:181], v192 offset:32768
	ds_read_b128 v[182:185], v192 offset:33792
	ds_read_b128 v[194:197], v192 offset:34816
	ds_read_b128 v[198:201], v192 offset:35840
	ds_read_b128 v[202:205], v192 offset:36864
	ds_read_b128 v[206:209], v192 offset:37888
	ds_read_b128 v[210:213], v192 offset:38912
	ds_read_b128 v[214:217], v192 offset:39936
	global_load_lds_dwordx4 v[224:225], off
	v_lshl_add_u64 v[224:225], s[38:39], 0, v[150:151]
	s_mov_b32 m0, s46
	s_nop 0
	global_load_lds_dwordx4 v[224:225], off
	s_waitcnt vmcnt(8)
	s_waitcnt lgkmcnt(0)
	s_barrier
	s_setprio 1
	s_waitcnt lgkmcnt(0)
	v_mfma_f32_16x16x32_bf16 v[126:129], v[130:133], v[178:181], v[126:129]
	v_mfma_f32_16x16x32_bf16 v[122:125], v[138:141], v[178:181], v[122:125]
	v_mfma_f32_16x16x32_bf16 v[110:113], v[130:133], v[194:197], v[110:113]
	v_mfma_f32_16x16x32_bf16 v[106:109], v[138:141], v[194:197], v[106:109]
	v_mfma_f32_16x16x32_bf16 v[94:97], v[130:133], v[202:205], v[94:97]
	v_mfma_f32_16x16x32_bf16 v[90:93], v[138:141], v[202:205], v[90:93]
	v_mfma_f32_16x16x32_bf16 v[78:81], v[130:133], v[210:213], v[78:81]
	v_mfma_f32_16x16x32_bf16 v[74:77], v[138:141], v[210:213], v[74:77]
	v_mfma_f32_16x16x32_bf16 v[126:129], v[134:137], v[182:185], v[126:129]
	v_mfma_f32_16x16x32_bf16 v[122:125], v[142:145], v[182:185], v[122:125]
	v_mfma_f32_16x16x32_bf16 v[110:113], v[134:137], v[198:201], v[110:113]
	v_mfma_f32_16x16x32_bf16 v[106:109], v[142:145], v[198:201], v[106:109]
	v_mfma_f32_16x16x32_bf16 v[94:97], v[134:137], v[206:209], v[94:97]
	v_mfma_f32_16x16x32_bf16 v[90:93], v[142:145], v[206:209], v[90:93]
	v_mfma_f32_16x16x32_bf16 v[78:81], v[134:137], v[214:217], v[78:81]
	v_mfma_f32_16x16x32_bf16 v[74:77], v[142:145], v[214:217], v[74:77]
	s_setprio 0
	s_setprio 1
	v_mfma_f32_16x16x32_bf16 v[118:121], v[162:165], v[178:181], v[118:121]
	v_mfma_f32_16x16x32_bf16 v[114:117], v[170:173], v[178:181], v[114:117]
	v_mfma_f32_16x16x32_bf16 v[102:105], v[162:165], v[194:197], v[102:105]
	v_mfma_f32_16x16x32_bf16 v[98:101], v[170:173], v[194:197], v[98:101]
	v_mfma_f32_16x16x32_bf16 v[86:89], v[162:165], v[202:205], v[86:89]
	v_mfma_f32_16x16x32_bf16 v[82:85], v[170:173], v[202:205], v[82:85]
	v_mfma_f32_16x16x32_bf16 v[70:73], v[162:165], v[210:213], v[70:73]
	v_mfma_f32_16x16x32_bf16 v[66:69], v[170:173], v[210:213], v[66:69]
	v_mfma_f32_16x16x32_bf16 v[118:121], v[166:169], v[182:185], v[118:121]
	v_mfma_f32_16x16x32_bf16 v[114:117], v[174:177], v[182:185], v[114:117]
	v_mfma_f32_16x16x32_bf16 v[102:105], v[166:169], v[198:201], v[102:105]
	v_mfma_f32_16x16x32_bf16 v[98:101], v[174:177], v[198:201], v[98:101]
	v_mfma_f32_16x16x32_bf16 v[86:89], v[166:169], v[206:209], v[86:89]
	v_mfma_f32_16x16x32_bf16 v[82:85], v[174:177], v[206:209], v[82:85]
	v_mfma_f32_16x16x32_bf16 v[70:73], v[166:169], v[214:217], v[70:73]
	v_mfma_f32_16x16x32_bf16 v[66:69], v[174:177], v[214:217], v[66:69]
	s_setprio 0
	s_barrier
; #define PG8_STAGE(bufoff, gbase, voff) do { _Pragma("unroll") for (int _i = 0; _i < 2; ++_i) \
;         __builtin_amdgcn_global_load_lds((const unsigned*)((const char*)(gbase) + (voff)[_i]), (PG8_LAS unsigned*)(lds + (bufoff) + ldsw + _i * 8192), 16, 0, 0); } while (0)
; #define PG8_LDA(dst, b, h) do { _Pragma("unroll") for (int m = 0; m < 4; ++m) _Pragma("unroll") for (int k = 0; k < 2; ++k) dst[m][k] = *(const PG8_LAS bf16x8*)(lds + PG8_SA(b, h) + aoff + m * 2048 + k * 1024); } while (0)
; #define PG8_WAIT_V(n) asm volatile("s_waitcnt vmcnt(" #n ")" ::: "memory")
; #define PG8_WAIT_L(n) asm volatile("s_waitcnt lgkmcnt(" #n ")" ::: "memory")
; #define PG8_BAR __builtin_amdgcn_s_barrier()
; #define PG8_SCHED __builtin_amdgcn_sched_barrier(0)
; template <class Epi, class Sched, bool ALIGN_EPI = false, bool SP2 = false, bool FP8 = false>
; __device__ __forceinline__ void gemm_phase(PG8_LAS unsigned char* lds, const Gemm g, const Sched& S, const Epi& E) {
;     ...
;         for (int t = 0; t < nt; t += 2) {
;             const bool last = (t == nt - 2);
;             const char* a1 = cA + (size_t)(t + 1) * kstep;
;             const char* a2 = last ? nA : cA + (size_t)(t + 2) * kstep; const char* b2 = last ? nB : cB + (size_t)(t + 2) * kstep;
;     ...
;             PG8_LDA(At, 1, 1); PG8_STAGE(PG8_SB(1, 0), b3, voffB); PG8_STAGE(PG8_SB(1, 1), b3 + hstep, voffB); PG8_STAGE(PG8_SA(1, 0), a3, voffA);
;             PG8_WAIT_V(8); PG8_WAIT_L(0); PG8_BAR; PG8_MMA(1, 0, At, B0); PG8_MMA(1, 1, At, B1); PG8_BAR; PG8_SCHED;
	s_add_i32 s38, s70, s43
	v_lshl_add_u64 v[186:187], v[186:187], 0, s[10:11]
	s_mov_b32 m0, s38
	ds_read_b128 v[178:181], v192 offset:49152
	ds_read_b128 v[182:185], v192 offset:50176
	ds_read_b128 v[194:197], v192 offset:51200
	ds_read_b128 v[198:201], v192 offset:52224
	ds_read_b128 v[202:205], v192 offset:53248
	ds_read_b128 v[206:209], v192 offset:54272
	ds_read_b128 v[210:213], v192 offset:55296
	ds_read_b128 v[214:217], v192 offset:56320
	global_load_lds_dwordx4 v[186:187], off
	s_add_i32 m0, s38, 0x2000
	s_add_u32 s36, s36, 0x80080
	v_lshl_add_u64 v[186:187], v[218:219], 0, s[10:11]
	s_addc_u32 s37, s37, 0
	s_add_i32 s38, s71, s43
	global_load_lds_dwordx4 v[186:187], off
	v_lshl_add_u64 v[186:187], s[36:37], 0, v[148:149]
	s_mov_b32 m0, s38
	s_nop 0
	global_load_lds_dwordx4 v[186:187], off
	v_lshl_add_u64 v[186:187], s[36:37], 0, v[152:153]
	s_add_i32 m0, s38, 0x2000
	s_nop 0
	global_load_lds_dwordx4 v[186:187], off
	v_lshl_add_u64 v[186:187], v[220:221], 0, s[10:11]
	s_mov_b32 m0, s51
	s_nop 0
	global_load_lds_dwordx4 v[186:187], off
	v_lshl_add_u64 v[186:187], v[222:223], 0, s[10:11]
	s_mov_b32 m0, s52
	s_nop 0
	global_load_lds_dwordx4 v[186:187], off
	s_waitcnt vmcnt(8)
	s_waitcnt lgkmcnt(0)
	s_barrier
	s_setprio 1
	s_waitcnt lgkmcnt(0)
	v_mfma_f32_16x16x32_bf16 v[62:65], v[130:133], v[178:181], v[62:65]
	v_mfma_f32_16x16x32_bf16 v[58:61], v[138:141], v[178:181], v[58:61]
	v_mfma_f32_16x16x32_bf16 v[46:49], v[130:133], v[194:197], v[46:49]
	v_mfma_f32_16x16x32_bf16 v[42:45], v[138:141], v[194:197], v[42:45]
	v_mfma_f32_16x16x32_bf16 v[30:33], v[130:133], v[202:205], v[30:33]
	v_mfma_f32_16x16x32_bf16 v[26:29], v[138:141], v[202:205], v[26:29]
	v_mfma_f32_16x16x32_bf16 v[14:17], v[130:133], v[210:213], v[14:17]
	v_mfma_f32_16x16x32_bf16 v[10:13], v[138:141], v[210:213], v[10:13]
	v_mfma_f32_16x16x32_bf16 v[62:65], v[134:137], v[182:185], v[62:65]
	v_mfma_f32_16x16x32_bf16 v[58:61], v[142:145], v[182:185], v[58:61]
	v_mfma_f32_16x16x32_bf16 v[46:49], v[134:137], v[198:201], v[46:49]
	v_mfma_f32_16x16x32_bf16 v[42:45], v[142:145], v[198:201], v[42:45]
	v_mfma_f32_16x16x32_bf16 v[30:33], v[134:137], v[206:209], v[30:33]
	v_mfma_f32_16x16x32_bf16 v[26:29], v[142:145], v[206:209], v[26:29]
	v_mfma_f32_16x16x32_bf16 v[14:17], v[134:137], v[214:217], v[14:17]
	v_mfma_f32_16x16x32_bf16 v[10:13], v[142:145], v[214:217], v[10:13]
	s_setprio 0
	s_setprio 1
	v_mfma_f32_16x16x32_bf16 v[54:57], v[162:165], v[178:181], v[54:57]
	v_mfma_f32_16x16x32_bf16 v[50:53], v[170:173], v[178:181], v[50:53]
	v_mfma_f32_16x16x32_bf16 v[38:41], v[162:165], v[194:197], v[38:41]
	v_mfma_f32_16x16x32_bf16 v[34:37], v[170:173], v[194:197], v[34:37]
	v_mfma_f32_16x16x32_bf16 v[22:25], v[162:165], v[202:205], v[22:25]
	v_mfma_f32_16x16x32_bf16 v[18:21], v[170:173], v[202:205], v[18:21]
	v_mfma_f32_16x16x32_bf16 v[6:9], v[162:165], v[210:213], v[6:9]
	v_mfma_f32_16x16x32_bf16 v[2:5], v[170:173], v[210:213], v[2:5]
	v_mfma_f32_16x16x32_bf16 v[54:57], v[166:169], v[182:185], v[54:57]
	v_mfma_f32_16x16x32_bf16 v[50:53], v[174:177], v[182:185], v[50:53]
	v_mfma_f32_16x16x32_bf16 v[38:41], v[166:169], v[198:201], v[38:41]
	v_mfma_f32_16x16x32_bf16 v[34:37], v[174:177], v[198:201], v[34:37]
	v_mfma_f32_16x16x32_bf16 v[22:25], v[166:169], v[206:209], v[22:25]
	v_mfma_f32_16x16x32_bf16 v[18:21], v[174:177], v[206:209], v[18:21]
	v_mfma_f32_16x16x32_bf16 v[6:9], v[166:169], v[214:217], v[6:9]
	v_mfma_f32_16x16x32_bf16 v[2:5], v[174:177], v[214:217], v[2:5]
	s_setprio 0
	s_add_i32 s69, s69, 2
	s_add_u32 s34, s34, 0x100
	s_addc_u32 s35, s35, 0
	s_add_u32 s63, s63, 0x100
	s_addc_u32 s68, s68, 0
	s_cmp_gt_u32 s69, 29
	s_barrier
	s_cbranch_scc0 .LBB0_1952
	s_and_b64 vcc, exec, s[12:13]
	s_cbranch_vccz .LBB0_1955
	s_barrier

; #define PG8_STAGE(bufoff, gbase, voff) do { _Pragma("unroll") for (int _i = 0; _i < 2; ++_i) \
;         __builtin_amdgcn_global_load_lds((const unsigned*)((const char*)(gbase) + (voff)[_i]), (PG8_LAS unsigned*)(lds + (bufoff) + ldsw + _i * 8192), 16, 0, 0); } while (0)
; #define PG8_LDA(dst, b, h) do { _Pragma("unroll") for (int m = 0; m < 4; ++m) _Pragma("unroll") for (int k = 0; k < 2; ++k) dst[m][k] = *(const PG8_LAS bf16x8*)(lds + PG8_SA(b, h) + aoff + m * 2048 + k * 1024); } while (0)
; #define PG8_LDB(dst, b, h) do { _Pragma("unroll") for (int n = 0; n < 2; ++n) _Pragma("unroll") for (int k = 0; k < 2; ++k) dst[n][k] = *(const PG8_LAS bf16x8*)(lds + PG8_SB(b, h) + boff + n * 2048 + k * 1024); } while (0)
; #define PG8_WAIT_V(n) asm volatile("s_waitcnt vmcnt(" #n ")" ::: "memory")
; #define PG8_WAIT_L(n) asm volatile("s_waitcnt lgkmcnt(" #n ")" ::: "memory")
; #define PG8_BAR __builtin_amdgcn_s_barrier()
; #define PG8_SCHED __builtin_amdgcn_sched_barrier(0)
; template <class Epi, class Sched, bool ALIGN_EPI = false, bool SP2 = false, bool FP8 = false>
; __device__ __forceinline__ void gemm_phase(PG8_LAS unsigned char* lds, const Gemm g, const Sched& S, const Epi& E) {
;     ...
;             PG8_LDB(B0, 0, 0); PG8_LDB(B1, 0, 1); PG8_SCHED; PG8_LDA(At, 0, 0); PG8_STAGE(PG8_SA(1, 1), a1 + hstep, voffA);
;             PG8_WAIT_V(8); PG8_WAIT_L(0); PG8_BAR; PG8_MMA(0, 0, At, B0); PG8_MMA(0, 1, At, B1); PG8_BAR; PG8_SCHED;
;             PG8_LDA(At, 0, 1); PG8_STAGE(PG8_SB(0, 0), b2, voffB); PG8_STAGE(PG8_SB(0, 1), b2 + hstep, voffB); PG8_STAGE(PG8_SA(0, 0), a2, voffA);
;             PG8_WAIT_V(8); PG8_WAIT_L(0); PG8_BAR; PG8_MMA(1, 0, At, B0); PG8_MMA(1, 1, At, B1); PG8_BAR; PG8_SCHED;
.LBB0_2184:
	ds_read_b128 v[26:29], v184
	ds_read_b128 v[30:33], v184 offset:1024
	ds_read_b128 v[18:21], v184 offset:2048
	ds_read_b128 v[22:25], v184 offset:3072
	ds_read_b128 v[10:13], v185
	ds_read_b128 v[14:17], v185 offset:1024
	ds_read_b128 v[2:5], v185 offset:2048
	ds_read_b128 v[6:9], v185 offset:3072
	s_add_u32 s26, s24, 0xfffc0080
	s_addc_u32 s27, s25, -1
	s_cmp_eq_u32 s60, 12
	s_cselect_b32 s29, s13, s27
	s_cselect_b32 s28, s56, s26
	s_cselect_b32 s27, s17, s59
	s_cselect_b32 s26, s57, s58
	v_lshl_add_u64 v[212:213], s[24:25], 0, v[170:171]
	s_add_i32 m0, s23, 0xc000
	ds_read_b128 v[174:177], v186
	ds_read_b128 v[178:181], v186 offset:1024
	ds_read_b128 v[188:191], v186 offset:2048
	ds_read_b128 v[192:195], v186 offset:3072
	ds_read_b128 v[196:199], v186 offset:4096
	ds_read_b128 v[200:203], v186 offset:5120
	ds_read_b128 v[204:207], v186 offset:6144
	ds_read_b128 v[208:211], v186 offset:7168
	global_load_lds_dwordx4 v[212:213], off
	v_lshl_add_u64 v[212:213], s[24:25], 0, v[172:173]
	s_add_i32 m0, s23, 0xe000
	s_nop 0
	global_load_lds_dwordx4 v[212:213], off
	s_waitcnt vmcnt(8)
	s_waitcnt lgkmcnt(0)
	s_barrier
	s_setprio 1
	s_waitcnt lgkmcnt(0)
	v_mfma_f32_16x16x128_f8f6f4 v[158:161], v[26:33], v[174:181], v[158:161]
	v_mfma_f32_16x16x128_f8f6f4 v[150:153], v[18:25], v[174:181], v[150:153]
	v_mfma_f32_16x16x128_f8f6f4 v[142:145], v[26:33], v[188:195], v[142:145]
	v_mfma_f32_16x16x128_f8f6f4 v[134:137], v[18:25], v[188:195], v[134:137]
	v_mfma_f32_16x16x128_f8f6f4 v[126:129], v[26:33], v[196:203], v[126:129]
	v_mfma_f32_16x16x128_f8f6f4 v[118:121], v[18:25], v[196:203], v[118:121]
	v_mfma_f32_16x16x128_f8f6f4 v[110:113], v[26:33], v[204:211], v[110:113]
	v_mfma_f32_16x16x128_f8f6f4 v[102:105], v[18:25], v[204:211], v[102:105]
	s_setprio 0
	s_setprio 1
	v_mfma_f32_16x16x128_f8f6f4 v[154:157], v[10:17], v[174:181], v[154:157]
	v_mfma_f32_16x16x128_f8f6f4 v[146:149], v[2:9], v[174:181], v[146:149]
	v_mfma_f32_16x16x128_f8f6f4 v[138:141], v[10:17], v[188:195], v[138:141]
	v_mfma_f32_16x16x128_f8f6f4 v[130:133], v[2:9], v[188:195], v[130:133]
	v_mfma_f32_16x16x128_f8f6f4 v[122:125], v[10:17], v[196:203], v[122:125]
	v_mfma_f32_16x16x128_f8f6f4 v[114:117], v[2:9], v[196:203], v[114:117]
	v_mfma_f32_16x16x128_f8f6f4 v[106:109], v[10:17], v[204:211], v[106:109]
	v_mfma_f32_16x16x128_f8f6f4 v[98:101], v[2:9], v[204:211], v[98:101]
	s_setprio 0
	s_barrier
	s_add_i32 s61, s51, s43
	v_lshl_add_u64 v[174:175], s[26:27], 0, v[162:163]
	s_mov_b32 m0, s61
	ds_read_b128 v[188:191], v186 offset:16384
	ds_read_b128 v[192:195], v186 offset:17408
	ds_read_b128 v[196:199], v186 offset:18432
	ds_read_b128 v[200:203], v186 offset:19456
	ds_read_b128 v[204:207], v186 offset:20480
	ds_read_b128 v[208:211], v186 offset:21504
	ds_read_b128 v[212:215], v186 offset:22528
	ds_read_b128 v[216:219], v186 offset:23552
	global_load_lds_dwordx4 v[174:175], off
	s_add_i32 m0, s61, 0x2000
	s_add_u32 s62, s26, 0x40000
	v_lshl_add_u64 v[176:177], s[26:27], 0, v[164:165]
	s_addc_u32 s63, s27, 0
	s_add_i32 s61, s52, s43
	global_load_lds_dwordx4 v[176:177], off
	v_lshl_add_u64 v[178:179], s[62:63], 0, v[162:163]
	s_mov_b32 m0, s61
	v_lshl_add_u64 v[180:181], s[28:29], 0, v[166:167]
	global_load_lds_dwordx4 v[178:179], off
	v_lshl_add_u64 v[178:179], s[62:63], 0, v[164:165]
	s_add_i32 m0, s61, 0x2000
	s_nop 0
	global_load_lds_dwordx4 v[178:179], off
	v_lshl_add_u64 v[178:179], s[28:29], 0, v[168:169]
	s_mov_b32 m0, s23
	s_nop 0
	global_load_lds_dwordx4 v[178:179], off
	s_mov_b32 m0, s44
	s_nop 0
	global_load_lds_dwordx4 v[180:181], off
	s_waitcnt vmcnt(8)
	s_waitcnt lgkmcnt(0)
	s_barrier
	s_setprio 1
	s_waitcnt lgkmcnt(0)
	v_mfma_f32_16x16x128_f8f6f4 v[94:97], v[26:33], v[188:195], v[94:97]
	v_mfma_f32_16x16x128_f8f6f4 v[86:89], v[18:25], v[188:195], v[86:89]
	v_mfma_f32_16x16x128_f8f6f4 v[78:81], v[26:33], v[196:203], v[78:81]
	v_mfma_f32_16x16x128_f8f6f4 v[70:73], v[18:25], v[196:203], v[70:73]
	v_mfma_f32_16x16x128_f8f6f4 v[62:65], v[26:33], v[204:211], v[62:65]
	v_mfma_f32_16x16x128_f8f6f4 v[54:57], v[18:25], v[204:211], v[54:57]
	v_mfma_f32_16x16x128_f8f6f4 v[46:49], v[26:33], v[212:219], v[46:49]
	v_mfma_f32_16x16x128_f8f6f4 v[38:41], v[18:25], v[212:219], v[38:41]
	s_setprio 0
	s_setprio 1
	v_mfma_f32_16x16x128_f8f6f4 v[90:93], v[10:17], v[188:195], v[90:93]
	v_mfma_f32_16x16x128_f8f6f4 v[82:85], v[2:9], v[188:195], v[82:85]
	v_mfma_f32_16x16x128_f8f6f4 v[74:77], v[10:17], v[196:203], v[74:77]
	v_mfma_f32_16x16x128_f8f6f4 v[66:69], v[2:9], v[196:203], v[66:69]
	v_mfma_f32_16x16x128_f8f6f4 v[58:61], v[10:17], v[204:211], v[58:61]
	v_mfma_f32_16x16x128_f8f6f4 v[50:53], v[2:9], v[204:211], v[50:53]
	v_mfma_f32_16x16x128_f8f6f4 v[42:45], v[10:17], v[212:219], v[42:45]
	v_mfma_f32_16x16x128_f8f6f4 v[34:37], v[2:9], v[212:219], v[34:37]
	s_setprio 0
	s_barrier
; #define PG8_STAGE(bufoff, gbase, voff) do { _Pragma("unroll") for (int _i = 0; _i < 2; ++_i) \
;         __builtin_amdgcn_global_load_lds((const unsigned*)((const char*)(gbase) + (voff)[_i]), (PG8_LAS unsigned*)(lds + (bufoff) + ldsw + _i * 8192), 16, 0, 0); } while (0)
; #define PG8_LDA(dst, b, h) do { _Pragma("unroll") for (int m = 0; m < 4; ++m) _Pragma("unroll") for (int k = 0; k < 2; ++k) dst[m][k] = *(const PG8_LAS bf16x8*)(lds + PG8_SA(b, h) + aoff + m * 2048 + k * 1024); } while (0)
; #define PG8_LDB(dst, b, h) do { _Pragma("unroll") for (int n = 0; n < 2; ++n) _Pragma("unroll") for (int k = 0; k < 2; ++k) dst[n][k] = *(const PG8_LAS bf16x8*)(lds + PG8_SB(b, h) + boff + n * 2048 + k * 1024); } while (0)
; #define PG8_WAIT_V(n) asm volatile("s_waitcnt vmcnt(" #n ")" ::: "memory")
; #define PG8_WAIT_L(n) asm volatile("s_waitcnt lgkmcnt(" #n ")" ::: "memory")
; #define PG8_BAR __builtin_amdgcn_s_barrier()
; #define PG8_SCHED __builtin_amdgcn_sched_barrier(0)
; template <class Epi, class Sched, bool ALIGN_EPI = false, bool SP2 = false, bool FP8 = false>
; __device__ __forceinline__ void gemm_phase(PG8_LAS unsigned char* lds, const Gemm g, const Sched& S, const Epi& E) {
;     ...
;         for (int t = 0; t < nt; t += 2) {
;             const bool last = (t == nt - 2);
;             const char* a1 = cA + (size_t)(t + 1) * kstep;
;             const char* a2 = last ? nA : cA + (size_t)(t + 2) * kstep; const char* b2 = last ? nB : cB + (size_t)(t + 2) * kstep;
;     ...
;             PG8_LDB(B0, 1, 0); PG8_LDB(B1, 1, 1); PG8_SCHED; PG8_LDA(At, 1, 0); PG8_STAGE(PG8_SA(0, 1), a2 + hstep, voffA);
;             PG8_WAIT_V(8); PG8_WAIT_L(0); PG8_BAR; PG8_MMA(0, 0, At, B0); PG8_MMA(0, 1, At, B1); PG8_BAR; PG8_SCHED;
;             PG8_LDA(At, 1, 1); PG8_STAGE(PG8_SB(1, 0), b3, voffB); PG8_STAGE(PG8_SB(1, 1), b3 + hstep, voffB); PG8_STAGE(PG8_SA(1, 0), a3, voffA);
;             PG8_WAIT_V(8); PG8_WAIT_L(0); PG8_BAR; PG8_MMA(1, 0, At, B0); PG8_MMA(1, 1, At, B1); PG8_BAR; PG8_SCHED;
;     ...
;         if constexpr (FP8) asm volatile("s_nop 15\n\ts_nop 15\n\ts_nop 15\n\ts_nop 15" ::: "memory");
	s_add_i32 s61, 0, 0x18000
	s_add_i32 s62, 0, 0x1c000
	v_add_u32_e32 v14, s61, v182
	v_add_u32_e32 v30, s62, v182
	ds_read_b128 v[2:5], v14
	ds_read_b128 v[6:9], v14 offset:1024
	ds_read_b128 v[10:13], v14 offset:2048
	ds_read_b128 v[14:17], v14 offset:3072
	ds_read_b128 v[18:21], v30
	ds_read_b128 v[22:25], v30 offset:1024
	ds_read_b128 v[26:29], v30 offset:2048
	ds_read_b128 v[30:33], v30 offset:3072
	s_add_u32 s28, s28, 0x40000
	s_addc_u32 s29, s29, 0
	s_mov_b32 m0, s45
	v_lshl_add_u64 v[220:221], s[28:29], 0, v[168:169]
	ds_read_b128 v[188:191], v186 offset:32768
	ds_read_b128 v[192:195], v186 offset:33792
	ds_read_b128 v[196:199], v186 offset:34816
	ds_read_b128 v[200:203], v186 offset:35840
	ds_read_b128 v[204:207], v186 offset:36864
	ds_read_b128 v[208:211], v186 offset:37888
	ds_read_b128 v[212:215], v186 offset:38912
	ds_read_b128 v[216:219], v186 offset:39936
	global_load_lds_dwordx4 v[220:221], off
	v_lshl_add_u64 v[220:221], s[28:29], 0, v[166:167]
	s_mov_b32 m0, s46
	s_nop 0
	global_load_lds_dwordx4 v[220:221], off
	s_waitcnt vmcnt(8)
	s_waitcnt lgkmcnt(0)
	s_barrier
	s_setprio 1
	s_waitcnt lgkmcnt(0)
	v_mfma_f32_16x16x128_f8f6f4 v[158:161], v[2:9], v[188:195], v[158:161]
	v_mfma_f32_16x16x128_f8f6f4 v[150:153], v[10:17], v[188:195], v[150:153]
	v_mfma_f32_16x16x128_f8f6f4 v[142:145], v[2:9], v[196:203], v[142:145]
	v_mfma_f32_16x16x128_f8f6f4 v[134:137], v[10:17], v[196:203], v[134:137]
	v_mfma_f32_16x16x128_f8f6f4 v[126:129], v[2:9], v[204:211], v[126:129]
	v_mfma_f32_16x16x128_f8f6f4 v[118:121], v[10:17], v[204:211], v[118:121]
	v_mfma_f32_16x16x128_f8f6f4 v[110:113], v[2:9], v[212:219], v[110:113]
	v_mfma_f32_16x16x128_f8f6f4 v[102:105], v[10:17], v[212:219], v[102:105]
	s_setprio 0
	s_setprio 1
	v_mfma_f32_16x16x128_f8f6f4 v[154:157], v[18:25], v[188:195], v[154:157]
	v_mfma_f32_16x16x128_f8f6f4 v[146:149], v[26:33], v[188:195], v[146:149]
	v_mfma_f32_16x16x128_f8f6f4 v[138:141], v[18:25], v[196:203], v[138:141]
	v_mfma_f32_16x16x128_f8f6f4 v[130:133], v[26:33], v[196:203], v[130:133]
	v_mfma_f32_16x16x128_f8f6f4 v[122:125], v[18:25], v[204:211], v[122:125]
	v_mfma_f32_16x16x128_f8f6f4 v[114:117], v[26:33], v[204:211], v[114:117]
	v_mfma_f32_16x16x128_f8f6f4 v[106:109], v[18:25], v[212:219], v[106:109]
	v_mfma_f32_16x16x128_f8f6f4 v[98:101], v[26:33], v[212:219], v[98:101]
	s_setprio 0
	s_barrier
	s_add_i32 s28, s61, s43
	v_lshl_add_u64 v[174:175], v[174:175], 0, s[6:7]
	s_mov_b32 m0, s28
	ds_read_b128 v[188:191], v186 offset:49152
	ds_read_b128 v[192:195], v186 offset:50176
	ds_read_b128 v[196:199], v186 offset:51200
	ds_read_b128 v[200:203], v186 offset:52224
	ds_read_b128 v[204:207], v186 offset:53248
	ds_read_b128 v[208:211], v186 offset:54272
	ds_read_b128 v[212:215], v186 offset:55296
	ds_read_b128 v[216:219], v186 offset:56320
	global_load_lds_dwordx4 v[174:175], off
	s_add_i32 m0, s28, 0x2000
	s_add_u32 s26, s26, 0x40080
	v_lshl_add_u64 v[174:175], v[176:177], 0, s[6:7]
	s_addc_u32 s27, s27, 0
	s_add_i32 s28, s62, s43
	global_load_lds_dwordx4 v[174:175], off
	v_lshl_add_u64 v[174:175], s[26:27], 0, v[162:163]
	s_mov_b32 m0, s28
	s_nop 0
	global_load_lds_dwordx4 v[174:175], off
	v_lshl_add_u64 v[174:175], s[26:27], 0, v[164:165]
	s_add_i32 m0, s28, 0x2000
	s_nop 0
	global_load_lds_dwordx4 v[174:175], off
	v_lshl_add_u64 v[174:175], v[178:179], 0, s[6:7]
	s_mov_b32 m0, s49
	s_nop 0
	global_load_lds_dwordx4 v[174:175], off
	v_lshl_add_u64 v[174:175], v[180:181], 0, s[6:7]
	s_mov_b32 m0, s50
	s_nop 0
	global_load_lds_dwordx4 v[174:175], off
	s_waitcnt vmcnt(8)
	s_waitcnt lgkmcnt(0)
	s_barrier
	s_setprio 1
	s_waitcnt lgkmcnt(0)
	v_mfma_f32_16x16x128_f8f6f4 v[94:97], v[2:9], v[188:195], v[94:97]
	v_mfma_f32_16x16x128_f8f6f4 v[86:89], v[10:17], v[188:195], v[86:89]
	v_mfma_f32_16x16x128_f8f6f4 v[78:81], v[2:9], v[196:203], v[78:81]
	v_mfma_f32_16x16x128_f8f6f4 v[70:73], v[10:17], v[196:203], v[70:73]
	v_mfma_f32_16x16x128_f8f6f4 v[62:65], v[2:9], v[204:211], v[62:65]
	v_mfma_f32_16x16x128_f8f6f4 v[54:57], v[10:17], v[204:211], v[54:57]
	v_mfma_f32_16x16x128_f8f6f4 v[46:49], v[2:9], v[212:219], v[46:49]
	v_mfma_f32_16x16x128_f8f6f4 v[38:41], v[10:17], v[212:219], v[38:41]
	s_setprio 0
	s_setprio 1
	v_mfma_f32_16x16x128_f8f6f4 v[90:93], v[18:25], v[188:195], v[90:93]
	v_mfma_f32_16x16x128_f8f6f4 v[82:85], v[26:33], v[188:195], v[82:85]
	v_mfma_f32_16x16x128_f8f6f4 v[74:77], v[18:25], v[196:203], v[74:77]
	v_mfma_f32_16x16x128_f8f6f4 v[66:69], v[26:33], v[196:203], v[66:69]
	v_mfma_f32_16x16x128_f8f6f4 v[58:61], v[18:25], v[204:211], v[58:61]
	v_mfma_f32_16x16x128_f8f6f4 v[50:53], v[26:33], v[204:211], v[50:53]
	v_mfma_f32_16x16x128_f8f6f4 v[42:45], v[18:25], v[212:219], v[42:45]
	v_mfma_f32_16x16x128_f8f6f4 v[34:37], v[26:33], v[212:219], v[34:37]
	s_setprio 0
	s_add_i32 s60, s60, 2
	s_add_u32 s24, s24, 0x100
	s_addc_u32 s25, s25, 0
	s_add_u32 s58, s58, 0x100
	s_addc_u32 s59, s59, 0
	s_cmp_gt_u32 s60, 13
	s_barrier
	s_cbranch_scc0 .LBB0_2184
	s_nop 15
	s_nop 15
	s_nop 15
	s_nop 15
	s_and_b64 vcc, exec, s[8:9]
	s_cbranch_vccz .LBB0_2187
	s_barrier

; #define PG8_STAGE(bufoff, gbase, voff) do { _Pragma("unroll") for (int _i = 0; _i < 2; ++_i) \
;         __builtin_amdgcn_global_load_lds((const unsigned*)((const char*)(gbase) + (voff)[_i]), (PG8_LAS unsigned*)(lds + (bufoff) + ldsw + _i * 8192), 16, 0, 0); } while (0)
; #define PG8_LDA(dst, b, h) do { _Pragma("unroll") for (int m = 0; m < 4; ++m) _Pragma("unroll") for (int k = 0; k < 2; ++k) dst[m][k] = *(const PG8_LAS bf16x8*)(lds + PG8_SA(b, h) + aoff + m * 2048 + k * 1024); } while (0)
; #define PG8_LDB(dst, b, h) do { _Pragma("unroll") for (int n = 0; n < 2; ++n) _Pragma("unroll") for (int k = 0; k < 2; ++k) dst[n][k] = *(const PG8_LAS bf16x8*)(lds + PG8_SB(b, h) + boff + n * 2048 + k * 1024); } while (0)
; #define PG8_WAIT_V(n) asm volatile("s_waitcnt vmcnt(" #n ")" ::: "memory")
; #define PG8_WAIT_L(n) asm volatile("s_waitcnt lgkmcnt(" #n ")" ::: "memory")
; #define PG8_BAR __builtin_amdgcn_s_barrier()
; #define PG8_SCHED __builtin_amdgcn_sched_barrier(0)
; template <class Epi, class Sched, bool ALIGN_EPI = false, bool SP2 = false, bool FP8 = false>
; __device__ __forceinline__ void gemm_phase(PG8_LAS unsigned char* lds, const Gemm g, const Sched& S, const Epi& E) {
;     ...
;             PG8_LDB(B0, 0, 0); PG8_LDB(B1, 0, 1); PG8_SCHED; PG8_LDA(At, 0, 0); PG8_STAGE(PG8_SA(1, 1), a1 + hstep, voffA);
;             PG8_WAIT_V(8); PG8_WAIT_L(0); PG8_BAR; PG8_MMA(0, 0, At, B0); PG8_MMA(0, 1, At, B1); PG8_BAR; PG8_SCHED;
;             PG8_LDA(At, 0, 1); PG8_STAGE(PG8_SB(0, 0), b2, voffB); PG8_STAGE(PG8_SB(0, 1), b2 + hstep, voffB); PG8_STAGE(PG8_SA(0, 0), a2, voffA);
;             PG8_WAIT_V(8); PG8_WAIT_L(0); PG8_BAR; PG8_MMA(1, 0, At, B0); PG8_MMA(1, 1, At, B1); PG8_BAR; PG8_SCHED;
.LBB0_2259:
	ds_read_b128 v[26:29], v186
	ds_read_b128 v[30:33], v186 offset:1024
	ds_read_b128 v[18:21], v186 offset:2048
	ds_read_b128 v[22:25], v186 offset:3072
	ds_read_b128 v[10:13], v187
	ds_read_b128 v[14:17], v187 offset:1024
	ds_read_b128 v[2:5], v187 offset:2048
	ds_read_b128 v[6:9], v187 offset:3072
	s_add_u32 s36, s34, 0xfff20080
	s_addc_u32 s37, s35, -1
	s_cmp_eq_u32 s71, 52
	s_cselect_b64 vcc, -1, 0
	s_cselect_b32 s37, s31, s37
	s_cselect_b32 s36, s30, s36
	v_cndmask_b32_e32 v175, v173, v171, vcc
	v_cndmask_b32_e32 v174, v172, v170, vcc
	v_lshl_add_u64 v[214:215], s[34:35], 0, v[166:167]
	s_add_i32 m0, s48, 0xc000
	ds_read_b128 v[176:179], v188
	ds_read_b128 v[180:183], v188 offset:1024
	ds_read_b128 v[190:193], v188 offset:2048
	ds_read_b128 v[194:197], v188 offset:3072
	ds_read_b128 v[198:201], v188 offset:4096
	ds_read_b128 v[202:205], v188 offset:5120
	ds_read_b128 v[206:209], v188 offset:6144
	ds_read_b128 v[210:213], v188 offset:7168
	global_load_lds_dwordx4 v[214:215], off
	v_lshl_add_u64 v[214:215], s[34:35], 0, v[168:169]
	s_add_i32 m0, s48, 0xe000
	s_nop 0
	global_load_lds_dwordx4 v[214:215], off
	s_waitcnt vmcnt(8)
	s_waitcnt lgkmcnt(0)
	s_barrier
	s_setprio 1
	s_waitcnt lgkmcnt(0)
	v_mfma_f32_16x16x128_f8f6f4 v[158:161], v[26:33], v[176:183], v[158:161]
	v_mfma_f32_16x16x128_f8f6f4 v[154:157], v[18:25], v[176:183], v[154:157]
	v_mfma_f32_16x16x128_f8f6f4 v[146:149], v[26:33], v[190:197], v[146:149]
	v_mfma_f32_16x16x128_f8f6f4 v[138:141], v[18:25], v[190:197], v[138:141]
	v_mfma_f32_16x16x128_f8f6f4 v[130:133], v[26:33], v[198:205], v[130:133]
	v_mfma_f32_16x16x128_f8f6f4 v[122:125], v[18:25], v[198:205], v[122:125]
	v_mfma_f32_16x16x128_f8f6f4 v[114:117], v[26:33], v[206:213], v[114:117]
	v_mfma_f32_16x16x128_f8f6f4 v[106:109], v[18:25], v[206:213], v[106:109]
	s_setprio 0
	s_setprio 1
	v_mfma_f32_16x16x128_f8f6f4 v[150:153], v[10:17], v[176:183], v[150:153]
	v_mfma_f32_16x16x128_f8f6f4 v[142:145], v[2:9], v[176:183], v[142:145]
	v_mfma_f32_16x16x128_f8f6f4 v[134:137], v[10:17], v[190:197], v[134:137]
	v_mfma_f32_16x16x128_f8f6f4 v[126:129], v[2:9], v[190:197], v[126:129]
	v_mfma_f32_16x16x128_f8f6f4 v[118:121], v[10:17], v[198:205], v[118:121]
	v_mfma_f32_16x16x128_f8f6f4 v[110:113], v[2:9], v[198:205], v[110:113]
	v_mfma_f32_16x16x128_f8f6f4 v[102:105], v[10:17], v[206:213], v[102:105]
	v_mfma_f32_16x16x128_f8f6f4 v[98:101], v[2:9], v[206:213], v[98:101]
	s_setprio 0
	s_barrier
	s_add_i32 s72, s57, s47
	v_lshl_add_u64 v[176:177], v[174:175], 0, v[162:163]
	s_mov_b32 m0, s72
	ds_read_b128 v[190:193], v188 offset:16384
	ds_read_b128 v[194:197], v188 offset:17408
	ds_read_b128 v[198:201], v188 offset:18432
	ds_read_b128 v[202:205], v188 offset:19456
	ds_read_b128 v[206:209], v188 offset:20480
	ds_read_b128 v[210:213], v188 offset:21504
	ds_read_b128 v[214:217], v188 offset:22528
	ds_read_b128 v[218:221], v188 offset:23552
	global_load_lds_dwordx4 v[176:177], off
	v_lshl_add_u64 v[178:179], v[174:175], 0, v[164:165]
	s_add_i32 m0, s72, 0x2000
	v_lshl_add_u64 v[180:181], v[174:175], 0, s[6:7]
	s_add_i32 s72, s58, s47
	global_load_lds_dwordx4 v[178:179], off
	v_lshl_add_u64 v[182:183], v[180:181], 0, v[162:163]
	s_mov_b32 m0, s72
	v_lshl_add_u64 v[180:181], v[180:181], 0, v[164:165]
	global_load_lds_dwordx4 v[182:183], off
	s_add_i32 m0, s72, 0x2000
	v_lshl_add_u64 v[182:183], s[36:37], 0, v[164:165]
	global_load_lds_dwordx4 v[180:181], off
	v_lshl_add_u64 v[180:181], s[36:37], 0, v[162:163]
	s_mov_b32 m0, s48
	s_nop 0
	global_load_lds_dwordx4 v[180:181], off
	s_mov_b32 m0, s49
	s_nop 0
	global_load_lds_dwordx4 v[182:183], off
	s_waitcnt vmcnt(8)
	s_waitcnt lgkmcnt(0)
	s_barrier
	s_setprio 1
	s_waitcnt lgkmcnt(0)
	v_mfma_f32_16x16x128_f8f6f4 v[94:97], v[26:33], v[190:197], v[94:97]
	v_mfma_f32_16x16x128_f8f6f4 v[90:93], v[18:25], v[190:197], v[90:93]
	v_mfma_f32_16x16x128_f8f6f4 v[82:85], v[26:33], v[198:205], v[82:85]
	v_mfma_f32_16x16x128_f8f6f4 v[74:77], v[18:25], v[198:205], v[74:77]
	v_mfma_f32_16x16x128_f8f6f4 v[66:69], v[26:33], v[206:213], v[66:69]
	v_mfma_f32_16x16x128_f8f6f4 v[58:61], v[18:25], v[206:213], v[58:61]
	v_mfma_f32_16x16x128_f8f6f4 v[50:53], v[26:33], v[214:221], v[50:53]
	v_mfma_f32_16x16x128_f8f6f4 v[42:45], v[18:25], v[214:221], v[42:45]
	s_setprio 0
	s_setprio 1
	v_mfma_f32_16x16x128_f8f6f4 v[86:89], v[10:17], v[190:197], v[86:89]
	v_mfma_f32_16x16x128_f8f6f4 v[78:81], v[2:9], v[190:197], v[78:81]
	v_mfma_f32_16x16x128_f8f6f4 v[70:73], v[10:17], v[198:205], v[70:73]
	v_mfma_f32_16x16x128_f8f6f4 v[62:65], v[2:9], v[198:205], v[62:65]
	v_mfma_f32_16x16x128_f8f6f4 v[54:57], v[10:17], v[206:213], v[54:57]
	v_mfma_f32_16x16x128_f8f6f4 v[46:49], v[2:9], v[206:213], v[46:49]
	v_mfma_f32_16x16x128_f8f6f4 v[38:41], v[10:17], v[214:221], v[38:41]
	v_mfma_f32_16x16x128_f8f6f4 v[34:37], v[2:9], v[214:221], v[34:37]
	s_setprio 0
	s_barrier
; #define PG8_STAGE(bufoff, gbase, voff) do { _Pragma("unroll") for (int _i = 0; _i < 2; ++_i) \
;         __builtin_amdgcn_global_load_lds((const unsigned*)((const char*)(gbase) + (voff)[_i]), (PG8_LAS unsigned*)(lds + (bufoff) + ldsw + _i * 8192), 16, 0, 0); } while (0)
; #define PG8_LDA(dst, b, h) do { _Pragma("unroll") for (int m = 0; m < 4; ++m) _Pragma("unroll") for (int k = 0; k < 2; ++k) dst[m][k] = *(const PG8_LAS bf16x8*)(lds + PG8_SA(b, h) + aoff + m * 2048 + k * 1024); } while (0)
; #define PG8_LDB(dst, b, h) do { _Pragma("unroll") for (int n = 0; n < 2; ++n) _Pragma("unroll") for (int k = 0; k < 2; ++k) dst[n][k] = *(const PG8_LAS bf16x8*)(lds + PG8_SB(b, h) + boff + n * 2048 + k * 1024); } while (0)
; #define PG8_WAIT_V(n) asm volatile("s_waitcnt vmcnt(" #n ")" ::: "memory")
; #define PG8_WAIT_L(n) asm volatile("s_waitcnt lgkmcnt(" #n ")" ::: "memory")
; #define PG8_BAR __builtin_amdgcn_s_barrier()
; #define PG8_SCHED __builtin_amdgcn_sched_barrier(0)
; template <class Epi, class Sched, bool ALIGN_EPI = false, bool SP2 = false, bool FP8 = false>
; __device__ __forceinline__ void gemm_phase(PG8_LAS unsigned char* lds, const Gemm g, const Sched& S, const Epi& E) {
;     ...
;         for (int t = 0; t < nt; t += 2) {
;             const bool last = (t == nt - 2);
;             const char* a1 = cA + (size_t)(t + 1) * kstep;
;             const char* a2 = last ? nA : cA + (size_t)(t + 2) * kstep; const char* b2 = last ? nB : cB + (size_t)(t + 2) * kstep;
;     ...
;             PG8_LDB(B0, 1, 0); PG8_LDB(B1, 1, 1); PG8_SCHED; PG8_LDA(At, 1, 0); PG8_STAGE(PG8_SA(0, 1), a2 + hstep, voffA);
;             PG8_WAIT_V(8); PG8_WAIT_L(0); PG8_BAR; PG8_MMA(0, 0, At, B0); PG8_MMA(0, 1, At, B1); PG8_BAR; PG8_SCHED;
;             PG8_LDA(At, 1, 1); PG8_STAGE(PG8_SB(1, 0), b3, voffB); PG8_STAGE(PG8_SB(1, 1), b3 + hstep, voffB); PG8_STAGE(PG8_SA(1, 0), a3, voffA);
;             PG8_WAIT_V(8); PG8_WAIT_L(0); PG8_BAR; PG8_MMA(1, 0, At, B0); PG8_MMA(1, 1, At, B1); PG8_BAR; PG8_SCHED;
;     ...
;         if constexpr (FP8) asm volatile("s_nop 15\n\ts_nop 15\n\ts_nop 15\n\ts_nop 15" ::: "memory");
	s_add_i32 s72, 0, 0x18000
	s_add_i32 s73, 0, 0x1c000
	v_add_u32_e32 v14, s72, v184
	v_add_u32_e32 v30, s73, v184
	ds_read_b128 v[2:5], v14
	ds_read_b128 v[6:9], v14 offset:1024
	ds_read_b128 v[10:13], v14 offset:2048
	ds_read_b128 v[14:17], v14 offset:3072
	ds_read_b128 v[18:21], v30
	ds_read_b128 v[22:25], v30 offset:1024
	ds_read_b128 v[26:29], v30 offset:2048
	ds_read_b128 v[30:33], v30 offset:3072
	s_add_u32 s36, s36, 0xe0000
	s_addc_u32 s37, s37, 0
	s_mov_b32 m0, s50
	v_lshl_add_u64 v[222:223], s[36:37], 0, v[162:163]
	ds_read_b128 v[190:193], v188 offset:32768
	ds_read_b128 v[194:197], v188 offset:33792
	ds_read_b128 v[198:201], v188 offset:34816
	ds_read_b128 v[202:205], v188 offset:35840
	ds_read_b128 v[206:209], v188 offset:36864
	ds_read_b128 v[210:213], v188 offset:37888
	ds_read_b128 v[214:217], v188 offset:38912
	ds_read_b128 v[218:221], v188 offset:39936
	global_load_lds_dwordx4 v[222:223], off
	v_lshl_add_u64 v[222:223], s[36:37], 0, v[164:165]
	s_mov_b32 m0, s51
	s_nop 0
	global_load_lds_dwordx4 v[222:223], off
	s_waitcnt vmcnt(8)
	s_waitcnt lgkmcnt(0)
	s_barrier
	s_setprio 1
	s_waitcnt lgkmcnt(0)
	v_mfma_f32_16x16x128_f8f6f4 v[158:161], v[2:9], v[190:197], v[158:161]
	v_mfma_f32_16x16x128_f8f6f4 v[154:157], v[10:17], v[190:197], v[154:157]
	v_mfma_f32_16x16x128_f8f6f4 v[146:149], v[2:9], v[198:205], v[146:149]
	v_mfma_f32_16x16x128_f8f6f4 v[138:141], v[10:17], v[198:205], v[138:141]
	v_mfma_f32_16x16x128_f8f6f4 v[130:133], v[2:9], v[206:213], v[130:133]
	v_mfma_f32_16x16x128_f8f6f4 v[122:125], v[10:17], v[206:213], v[122:125]
	v_mfma_f32_16x16x128_f8f6f4 v[114:117], v[2:9], v[214:221], v[114:117]
	v_mfma_f32_16x16x128_f8f6f4 v[106:109], v[10:17], v[214:221], v[106:109]
	s_setprio 0
	s_setprio 1
	v_mfma_f32_16x16x128_f8f6f4 v[150:153], v[18:25], v[190:197], v[150:153]
	v_mfma_f32_16x16x128_f8f6f4 v[142:145], v[26:33], v[190:197], v[142:145]
	v_mfma_f32_16x16x128_f8f6f4 v[134:137], v[18:25], v[198:205], v[134:137]
	v_mfma_f32_16x16x128_f8f6f4 v[126:129], v[26:33], v[198:205], v[126:129]
	v_mfma_f32_16x16x128_f8f6f4 v[118:121], v[18:25], v[206:213], v[118:121]
	v_mfma_f32_16x16x128_f8f6f4 v[110:113], v[26:33], v[206:213], v[110:113]
	v_mfma_f32_16x16x128_f8f6f4 v[102:105], v[18:25], v[214:221], v[102:105]
	v_mfma_f32_16x16x128_f8f6f4 v[98:101], v[26:33], v[214:221], v[98:101]
	s_setprio 0
	s_barrier
	s_add_i32 s36, s72, s47
	v_lshl_add_u64 v[176:177], v[176:177], 0, s[12:13]
	s_mov_b32 m0, s36
	ds_read_b128 v[190:193], v188 offset:49152
	ds_read_b128 v[194:197], v188 offset:50176
	ds_read_b128 v[198:201], v188 offset:51200
	ds_read_b128 v[202:205], v188 offset:52224
	ds_read_b128 v[206:209], v188 offset:53248
	ds_read_b128 v[210:213], v188 offset:54272
	ds_read_b128 v[214:217], v188 offset:55296
	ds_read_b128 v[218:221], v188 offset:56320
	global_load_lds_dwordx4 v[176:177], off
	v_lshl_add_u64 v[176:177], v[178:179], 0, s[12:13]
	s_add_i32 m0, s36, 0x2000
	v_lshl_add_u64 v[174:175], v[174:175], 0, s[14:15]
	s_add_i32 s36, s73, s47
	global_load_lds_dwordx4 v[176:177], off
	v_lshl_add_u64 v[176:177], v[174:175], 0, v[162:163]
	s_mov_b32 m0, s36
	v_lshl_add_u64 v[174:175], v[174:175], 0, v[164:165]
	global_load_lds_dwordx4 v[176:177], off
	s_add_i32 m0, s36, 0x2000
	s_nop 0
	global_load_lds_dwordx4 v[174:175], off
	v_lshl_add_u64 v[174:175], v[180:181], 0, s[12:13]
	s_mov_b32 m0, s55
	s_nop 0
	global_load_lds_dwordx4 v[174:175], off
	v_lshl_add_u64 v[174:175], v[182:183], 0, s[12:13]
	s_mov_b32 m0, s56
	s_nop 0
	global_load_lds_dwordx4 v[174:175], off
	s_waitcnt vmcnt(8)
	s_waitcnt lgkmcnt(0)
	s_barrier
	s_setprio 1
	s_waitcnt lgkmcnt(0)
	v_mfma_f32_16x16x128_f8f6f4 v[94:97], v[2:9], v[190:197], v[94:97]
	v_mfma_f32_16x16x128_f8f6f4 v[90:93], v[10:17], v[190:197], v[90:93]
	v_mfma_f32_16x16x128_f8f6f4 v[82:85], v[2:9], v[198:205], v[82:85]
	v_mfma_f32_16x16x128_f8f6f4 v[74:77], v[10:17], v[198:205], v[74:77]
	v_mfma_f32_16x16x128_f8f6f4 v[66:69], v[2:9], v[206:213], v[66:69]
	v_mfma_f32_16x16x128_f8f6f4 v[58:61], v[10:17], v[206:213], v[58:61]
	v_mfma_f32_16x16x128_f8f6f4 v[50:53], v[2:9], v[214:221], v[50:53]
	v_mfma_f32_16x16x128_f8f6f4 v[42:45], v[10:17], v[214:221], v[42:45]
	s_setprio 0
	s_setprio 1
	v_mfma_f32_16x16x128_f8f6f4 v[86:89], v[18:25], v[190:197], v[86:89]
	v_mfma_f32_16x16x128_f8f6f4 v[78:81], v[26:33], v[190:197], v[78:81]
	v_mfma_f32_16x16x128_f8f6f4 v[70:73], v[18:25], v[198:205], v[70:73]
	v_mfma_f32_16x16x128_f8f6f4 v[62:65], v[26:33], v[198:205], v[62:65]
	v_mfma_f32_16x16x128_f8f6f4 v[54:57], v[18:25], v[206:213], v[54:57]
	v_mfma_f32_16x16x128_f8f6f4 v[46:49], v[26:33], v[206:213], v[46:49]
	v_mfma_f32_16x16x128_f8f6f4 v[38:41], v[18:25], v[214:221], v[38:41]
	v_mfma_f32_16x16x128_f8f6f4 v[34:37], v[26:33], v[214:221], v[34:37]
	s_setprio 0
	s_add_i32 s71, s71, 2
	s_add_u32 s34, s34, 0x100
	s_addc_u32 s35, s35, 0
	s_cmp_gt_u32 s71, 53
	v_lshl_add_u64 v[172:173], v[172:173], 0, s[18:19]
	s_barrier
	s_cbranch_scc0 .LBB0_2259
	s_nop 15
	s_nop 15
	s_nop 15
	s_nop 15
	s_and_b64 vcc, exec, s[16:17]
	s_cbranch_vccz .LBB0_2262
	s_barrier
